# hg_c: lb loads first, prefetch on every chunk, counted vmcnt waits at first consumers instead of chunk-top vmcnt(0)
# baseline (speedup 1.0000x reference)
; #define LAS __attribute__((address_space(3)))
; __device__ __forceinline__ float sigmoidf_(float x) { return __builtin_amdgcn_rcpf(1.0f + __expf(-x)); }
; template <bool WITHO, bool RAW = false>
; __device__ __forceinline__ void hg_pass(const Frame& F, const bf16_t* P, const float* lbh, int b, int h, int nb, int dir, f32x4 (&S)[4][4], float (&Gsum)[16],
;                                         LAS bf16_t* Vl, LAS bf16_t* Kl, float* OF, const float* ngp) {
;     ...
;     for (int ci = 0; ci < HG_U / 16; ++ci) {
;         float kk[16], c[16];
;         if (WITHO) { const int pos = ci * 16 + tau, t = dir ? (HG_U - 1 - pos) : pos; const bf16_t* pr = P + (size_t)hg_row(b, nb, t) * 4096 + h * 64 + 4 * g;
; #pragma unroll
;             for (int m = 0; m < 4; ++m) qr[m] = *(const u32x2*)(pr + 1536 + 16 * m); }
; #pragma unroll
;         for (int m = 0; m < 4; ++m) { const float z0 = __uint_as_float(zr[m].x << 16), z1 = __uint_as_float(zr[m].x & 0xffff0000u), z2 = __uint_as_float(zr[m].y << 16), z3 = __uint_as_float(zr[m].y & 0xffff0000u);
;             const float zz[4] = {z0, z1, z2, z3};
;             const f32x4 lb4 = *(const f32x4*)(lbh + 16 * m + 4 * g);
; #pragma unroll
;             for (int i = 0; i < 4; ++i) { const float lb = lb4[i]; const float f = fmaxf(lb + (1.0f - lb) * sigmoidf_(zz[i]), 1e-30f); kk[m * 4 + i] = 1.0f - f; c[m * 4 + i] = __logf(f); }
;             *(LAS u32x2*)(Vl + tau * 64 + 16 * m + 4 * g) = vr[m];
;  }
;         if (ci + 1 < HG_U / 16) { const int pos = (ci + 1) * 16 + tau, t = dir ? (HG_U - 1 - pos) : pos; const bf16_t* pr = P + (size_t)hg_row(b, nb, t) * 4096 + h * 64 + 4 * g;
; #pragma unroll
;             for (int m = 0; m < 4; ++m) { zr[m] = *(const u32x2*)(pr + (dir ? 2560 : 2048) + 16 * m); vr[m] = *(const u32x2*)(pr + 3072 + 16 * m); } }
;     ...
; #pragma unroll
;         for (int kt = 0; kt < 4; ++kt) { f32x4 eg;
; #pragma unroll
;             for (int i = 0; i < 4; ++i) eg[i] = __expf(G[kt * 4 + i]);
; #pragma unroll
;             for (int vt = 0; vt < 4; ++vt) S[kt][vt] = __builtin_amdgcn_mfma_f32_16x16x32_bf16(Kf[kt], Vf[vt], S[kt][vt] * eg, 0, 0, 0); }
.LBB0_1169:
	s_waitcnt vmcnt(16)
	v_mul_f32_e32 v70, 0x3fb8aa3b, v227
	v_mul_f32_e32 v71, 0x3fb8aa3b, v228
	v_mul_f32_e32 v86, 0x3fb8aa3b, v226
	v_mul_f32_e32 v87, 0x3fb8aa3b, v225
	v_mov_b32_e32 v94, v2
	v_mov_b32_e32 v95, v2
	v_exp_f32_e32 v70, v70
	v_exp_f32_e32 v86, v86
	v_exp_f32_e32 v87, v87
	v_exp_f32_e32 v71, v71
	v_mov_b32_e32 v90, v2
	v_mov_b32_e32 v91, v2
	v_pk_mul_f32 v[6:7], v[6:7], v[86:87]
	v_pk_mul_f32 v[4:5], v[4:5], v[70:71]
	v_pk_mul_f32 v[10:11], v[10:11], v[86:87]
	v_pk_mul_f32 v[8:9], v[8:9], v[70:71]
	v_pk_mul_f32 v[14:15], v[14:15], v[86:87]
	v_pk_mul_f32 v[12:13], v[12:13], v[70:71]
	v_pk_mul_f32 v[18:19], v[18:19], v[86:87]
	v_pk_mul_f32 v[16:17], v[16:17], v[70:71]
	v_mul_f32_e32 v86, 0x3fb8aa3b, v221
	v_mfma_f32_16x16x32_bf16 v[4:7], v[92:95], v[0:3], v[4:7]
	v_mul_f32_e32 v70, 0x3fb8aa3b, v224
	v_mul_f32_e32 v71, 0x3fb8aa3b, v223
	v_exp_f32_e32 v70, v70
	v_mfma_f32_16x16x32_bf16 v[8:11], v[92:95], v[80:83], v[8:11]
	v_exp_f32_e32 v71, v71
	v_mov_b32_e32 v87, v2
	s_add_i32 s27, s27, 16
	v_mfma_f32_16x16x32_bf16 v[12:15], v[92:95], v[76:79], v[12:15]
	v_mul_f32_e64 v20, v20, v70
	v_mul_f32_e64 v21, v21, v71
	v_pk_mul_f32 v[24:25], v[24:25], v[70:71]
	v_pk_mul_f32 v[28:29], v[28:29], v[70:71]
	v_mfma_f32_16x16x32_bf16 v[16:19], v[92:95], v[72:75], v[16:19]
	v_exp_f32_e32 v92, v86
	v_mul_f32_e32 v86, 0x3fb8aa3b, v222
	v_exp_f32_e32 v93, v86
	v_pk_mul_f32 v[48:49], v[48:49], v[70:71]
	v_mul_f32_e32 v70, 0x3fb8aa3b, v220
	v_mul_f32_e32 v71, 0x3fb8aa3b, v219
	v_pk_mul_f32 v[22:23], v[22:23], v[92:93]
	v_pk_mul_f32 v[26:27], v[26:27], v[92:93]
	v_pk_mul_f32 v[30:31], v[30:31], v[92:93]
	v_pk_mul_f32 v[50:51], v[50:51], v[92:93]
	v_mfma_f32_16x16x32_bf16 v[20:23], v[88:91], v[0:3], v[20:23]
	v_mov_b32_e32 v86, v2
	s_add_i32 s26, s26, -16
	s_cmpk_lg_i32 s27, 0x80
	v_mfma_f32_16x16x32_bf16 v[24:27], v[88:91], v[80:83], v[24:27]
	v_mfma_f32_16x16x32_bf16 v[28:31], v[88:91], v[76:79], v[28:31]
	v_mfma_f32_16x16x32_bf16 v[48:51], v[88:91], v[72:75], v[48:51]
	v_exp_f32_e32 v88, v70
	v_mul_f32_e32 v70, 0x3fb8aa3b, v218
	v_exp_f32_e32 v90, v71
	v_mul_f32_e32 v71, 0x3fb8aa3b, v217
	v_exp_f32_e32 v91, v71
	v_exp_f32_e32 v89, v70
	v_mov_b32_e32 v70, v2
	v_mov_b32_e32 v71, v2
	v_pk_mul_f32 v[34:35], v[34:35], v[90:91]
	v_pk_mul_f32 v[32:33], v[32:33], v[88:89]
	v_pk_mul_f32 v[38:39], v[38:39], v[90:91]
	v_pk_mul_f32 v[36:37], v[36:37], v[88:89]
	v_pk_mul_f32 v[42:43], v[42:43], v[90:91]
	v_pk_mul_f32 v[40:41], v[40:41], v[88:89]
	v_pk_mul_f32 v[46:47], v[46:47], v[90:91]
	v_pk_mul_f32 v[44:45], v[44:45], v[88:89]
	v_mfma_f32_16x16x32_bf16 v[32:35], v[84:87], v[0:3], v[32:35]
	v_mov_b64_e32 v[90:91], v[148:149]
	v_mov_b64_e32 v[88:89], v[150:151]
	v_mfma_f32_16x16x32_bf16 v[36:39], v[84:87], v[80:83], v[36:39]
	v_mfma_f32_16x16x32_bf16 v[40:43], v[84:87], v[76:79], v[40:43]
	v_mfma_f32_16x16x32_bf16 v[44:47], v[84:87], v[72:75], v[44:47]
	v_mul_f32_e32 v84, 0x3fb8aa3b, v215
	v_mul_f32_e32 v85, 0x3fb8aa3b, v216
	v_mul_f32_e32 v86, 0x3fb8aa3b, v213
	v_mul_f32_e32 v87, 0x3fb8aa3b, v214
	v_exp_f32_e32 v84, v84
	v_exp_f32_e32 v86, v86
	v_exp_f32_e32 v87, v87
	v_exp_f32_e32 v85, v85
	v_pk_mul_f32 v[54:55], v[54:55], v[86:87]
	v_pk_mul_f32 v[52:53], v[52:53], v[84:85]
	v_pk_mul_f32 v[58:59], v[58:59], v[86:87]
	v_pk_mul_f32 v[56:57], v[56:57], v[84:85]
	v_pk_mul_f32 v[62:63], v[62:63], v[86:87]
	v_pk_mul_f32 v[60:61], v[60:61], v[84:85]
	v_pk_mul_f32 v[66:67], v[66:67], v[86:87]
	v_pk_mul_f32 v[64:65], v[64:65], v[84:85]
	v_mfma_f32_16x16x32_bf16 v[52:55], v[68:71], v[0:3], v[52:55]
	v_mov_b64_e32 v[86:87], v[152:153]
	v_mov_b64_e32 v[84:85], v[154:155]
	v_mfma_f32_16x16x32_bf16 v[56:59], v[68:71], v[80:83], v[56:59]
	v_mfma_f32_16x16x32_bf16 v[60:63], v[68:71], v[76:79], v[60:63]
	v_mfma_f32_16x16x32_bf16 v[64:67], v[68:71], v[72:75], v[64:67]
	s_cbranch_scc0 .LBB0_1164
.LBB0_1170:
	v_add_u32_e32 v92, s26, v192
	v_add_u32_e32 v3, s27, v112
	v_add_u32_e32 v0, 0x7f, v92
	v_cndmask_b32_e64 v0, v0, v3, s[0:1]
	v_add_u32_e32 v0, s25, v0
	v_ashrrev_i32_e32 v1, 31, v0
	v_lshlrev_b64 v[0:1], 13, v[0:1]
	global_load_dwordx4 v[80:83], v[146:147], off
	global_load_dwordx4 v[76:79], v[146:147], off offset:64
	global_load_dwordx4 v[72:75], v[146:147], off offset:128
	global_load_dwordx4 v[68:71], v[146:147], off offset:192
	v_lshl_add_u64 v[156:157], v[126:127], 0, v[0:1]
	global_load_dwordx2 v[0:1], v[156:157], off offset:3072
	global_load_dwordx2 v[98:99], v[156:157], off offset:3104
	global_load_dwordx2 v[96:97], v[156:157], off offset:3136
	global_load_dwordx2 v[94:95], v[156:157], off offset:3168
	v_add_u32_e32 v93, 0x8000, v191
	s_cmpk_eq_i32 s27, 0x70
	ds_write2_b64 v93, v[136:137], v[138:139] offset1:4
	ds_write2_b64 v93, v[140:141], v[142:143] offset0:8 offset1:12
	v_add_u32_e32 v3, 16, v3
	v_add_u32_e32 v92, 0x6f, v92
	v_cndmask_b32_e64 v3, v92, v3, s[0:1]
	v_add_u32_e32 v92, s25, v3
	v_ashrrev_i32_e32 v93, 31, v92
	v_lshlrev_b64 v[92:93], 13, v[92:93]
	v_lshl_add_u64 v[92:93], v[126:127], 0, v[92:93]
	v_lshl_add_u64 v[100:101], v[92:93], 0, s[64:65]
	v_add_co_u32_e32 v92, vcc, 0x1000, v92
	s_nop 1
	v_addc_co_u32_e32 v93, vcc, 0, v93, vcc
	global_load_dwordx2 v[148:149], v[100:101], off
	global_load_dwordx2 v[150:151], v[100:101], off offset:32
	global_load_dwordx2 v[152:153], v[100:101], off offset:64
	global_load_dwordx2 v[154:155], v[100:101], off offset:96
	global_load_dwordx2 v[136:137], v[92:93], off offset:2048
	global_load_dwordx2 v[138:139], v[92:93], off offset:2080
	global_load_dwordx2 v[140:141], v[92:93], off offset:2112
	global_load_dwordx2 v[142:143], v[92:93], off offset:2144
; #define LAS __attribute__((address_space(3)))
; __device__ __forceinline__ float sigmoidf_(float x) { return __builtin_amdgcn_rcpf(1.0f + __expf(-x)); }
; template <int CTRL> __device__ __forceinline__ float dpp_add0(float x) { return x + dppf<CTRL>(0.0f, x); }
; template <bool WITHO, bool RAW = false>
; __device__ __forceinline__ void hg_pass(const Frame& F, const bf16_t* P, const float* lbh, int b, int h, int nb, int dir, f32x4 (&S)[4][4], float (&Gsum)[16],
;                                         LAS bf16_t* Vl, LAS bf16_t* Kl, float* OF, const float* ngp) {
;     ...
;         for (int m = 0; m < 4; ++m) { const float z0 = __uint_as_float(zr[m].x << 16), z1 = __uint_as_float(zr[m].x & 0xffff0000u), z2 = __uint_as_float(zr[m].y << 16), z3 = __uint_as_float(zr[m].y & 0xffff0000u);
;             const float zz[4] = {z0, z1, z2, z3};
;             const f32x4 lb4 = *(const f32x4*)(lbh + 16 * m + 4 * g);
; #pragma unroll
;             for (int i = 0; i < 4; ++i) { const float lb = lb4[i]; const float f = fmaxf(lb + (1.0f - lb) * sigmoidf_(zz[i]), 1e-30f); kk[m * 4 + i] = 1.0f - f; c[m * 4 + i] = __logf(f); }
;             *(LAS u32x2*)(Vl + tau * 64 + 16 * m + 4 * g) = vr[m];
;  }
;         if (ci + 1 < HG_U / 16) { const int pos = (ci + 1) * 16 + tau, t = dir ? (HG_U - 1 - pos) : pos; const bf16_t* pr = P + (size_t)hg_row(b, nb, t) * 4096 + h * 64 + 4 * g;
; #pragma unroll
;             for (int m = 0; m < 4; ++m) { zr[m] = *(const u32x2*)(pr + (dir ? 2560 : 2048) + 16 * m); vr[m] = *(const u32x2*)(pr + 3072 + 16 * m); } }
;         float G[16];
; #pragma unroll
;         for (int q = 0; q < 16; ++q) G[q] = c[q];
; #pragma unroll
;         for (int q = 0; q < 16; q += 4) ROW_ALLREDUCE4(G[q], G[q + 1], G[q + 2], G[q + 3]);
; #pragma unroll
;         for (int q = 0; q < 16; ++q) { c[q] = dpp_add0<0x111>(c[q]); c[q] = dpp_add0<0x112>(c[q]); c[q] = dpp_add0<0x114>(c[q]); c[q] = dpp_add0<0x118>(c[q]); }
.LBB0_1172:
	v_lshlrev_b32_e32 v3, 16, v90
	v_mul_f32_e32 v3, 0xbfb8aa3b, v3
	v_exp_f32_e32 v3, v3
	s_waitcnt vmcnt(12)
	v_sub_f32_e32 v93, 1.0, v80
	v_and_b32_e32 v90, 0xffff0000, v90
	v_mul_f32_e32 v90, 0xbfb8aa3b, v90
	v_add_f32_e32 v3, 1.0, v3
	v_rcp_f32_e32 v3, v3
	v_exp_f32_e32 v90, v90
	v_lshlrev_b32_e32 v92, 16, v91
	v_and_b32_e32 v91, 0xffff0000, v91
	v_fma_f32 v3, v3, v93, v80
	v_max_f32_e32 v3, 0xda24260, v3
	v_add_f32_e32 v90, 1.0, v90
	v_sub_f32_e32 v100, 1.0, v3
	v_log_f32_e32 v80, v3
	v_rcp_f32_e32 v90, v90
	v_mul_f32_e32 v91, 0xbfb8aa3b, v91
	v_exp_f32_e32 v91, v91
	v_mul_f32_e32 v3, 0x3f317217, v80
	v_fma_f32 v3, v80, s93, -v3
	v_fmac_f32_e32 v3, 0x3377d1cf, v80
	v_fmac_f32_e32 v3, 0x3f317217, v80
	v_add_f32_e32 v91, 1.0, v91
	v_rcp_f32_e32 v91, v91
	v_sub_f32_e32 v80, 1.0, v81
	v_fma_f32 v80, v90, v80, v81
	v_max_f32_e32 v80, 0xda24260, v80
	v_mul_f32_e32 v90, 0xbfb8aa3b, v92
	v_log_f32_e32 v81, v80
	v_exp_f32_e32 v90, v90
	v_sub_f32_e32 v101, 1.0, v80
	v_lshlrev_b32_e32 v92, 16, v88
	v_mul_f32_e32 v80, 0x3f317217, v81
	v_add_f32_e32 v90, 1.0, v90
	v_fma_f32 v80, v81, s93, -v80
	v_rcp_f32_e32 v90, v90
	v_fmac_f32_e32 v80, 0x3377d1cf, v81
	v_fmac_f32_e32 v80, 0x3f317217, v81
	v_mul_f32_e32 v92, 0xbfb8aa3b, v92
	v_exp_f32_e32 v92, v92
	v_sub_f32_e32 v81, 1.0, v82
	v_fma_f32 v81, v90, v81, v82
	v_max_f32_e32 v81, 0xda24260, v81
	v_cmp_gt_f32_e32 vcc, s92, v81
	v_add_f32_e32 v92, 1.0, v92
	v_rcp_f32_e32 v92, v92
	v_cndmask_b32_e64 v82, 0, 32, vcc
	v_ldexp_f32 v82, v81, v82
	v_log_f32_e32 v90, v82
	v_sub_f32_e32 v82, 1.0, v81
	v_mul_f32_e32 v81, 0x3f317217, v90
	v_fma_f32 v81, v90, s93, -v81
	v_fmac_f32_e32 v81, 0x3377d1cf, v90
	v_fmac_f32_e32 v81, 0x3f317217, v90
	v_cmp_lt_f32_e64 s[48:49], |v90|, s90
	v_and_b32_e32 v88, 0xffff0000, v88
	v_mul_f32_e32 v88, 0xbfb8aa3b, v88
	v_cndmask_b32_e64 v81, v90, v81, s[48:49]
	v_sub_f32_e32 v90, 1.0, v83
	v_fmac_f32_e32 v83, v91, v90
	v_max_f32_e32 v83, 0xda24260, v83
	v_cndmask_b32_e32 v91, 0, v179, vcc
	v_sub_f32_e32 v81, v81, v91
	v_log_f32_e32 v90, v83
	v_exp_f32_e32 v88, v88
	v_mov_b32_e32 v227, v3
	v_add_f32_dpp v3, v3, v3 row_shr:1 row_mask:0xf bank_mask:0xf bound_ctrl:1
	v_mul_f32_e32 v91, 0x3f317217, v90
	v_fma_f32 v91, v90, s93, -v91
	v_fmac_f32_e32 v91, 0x3377d1cf, v90
	v_fmac_f32_e32 v91, 0x3f317217, v90
	v_add_f32_e32 v88, 1.0, v88
	v_rcp_f32_e32 v88, v88
	v_mov_b32_e32 v90, v91
	v_sub_f32_e32 v91, 1.0, v76
	v_fma_f32 v76, v92, v91, v76
	v_max_f32_e32 v76, 0xda24260, v76
	v_sub_f32_e32 v102, 1.0, v76
	v_lshlrev_b32_e32 v92, 16, v89
	v_log_f32_e32 v91, v76
	v_and_b32_e32 v89, 0xffff0000, v89
	v_mul_f32_e32 v89, 0xbfb8aa3b, v89
	v_exp_f32_e32 v89, v89
	v_mul_f32_e32 v76, 0x3f317217, v91
	v_fma_f32 v76, v91, s93, -v76
	v_fmac_f32_e32 v76, 0x3377d1cf, v91
	v_fmac_f32_e32 v76, 0x3f317217, v91
	v_add_f32_e32 v89, 1.0, v89
	v_rcp_f32_e32 v89, v89
	v_sub_f32_e32 v91, 1.0, v77
	v_fma_f32 v77, v88, v91, v77
	v_max_f32_e32 v77, 0xda24260, v77
	v_mul_f32_e32 v91, 0xbfb8aa3b, v92
	v_log_f32_e32 v88, v77
	v_exp_f32_e32 v91, v91
	v_sub_f32_e32 v103, 1.0, v77
	v_lshlrev_b32_e32 v92, 16, v84
	v_mul_f32_e32 v77, 0x3f317217, v88
	v_add_f32_e32 v91, 1.0, v91
	v_fma_f32 v77, v88, s93, -v77
	v_rcp_f32_e32 v91, v91
	v_fmac_f32_e32 v77, 0x3377d1cf, v88
	v_fmac_f32_e32 v77, 0x3f317217, v88
	v_mul_f32_e32 v92, 0xbfb8aa3b, v92
	v_exp_f32_e32 v92, v92
	v_sub_f32_e32 v88, 1.0, v78
	v_fma_f32 v78, v91, v88, v78
	v_max_f32_e32 v78, 0xda24260, v78
	v_sub_f32_e32 v104, 1.0, v78
	v_log_f32_e32 v88, v78
	v_lshlrev_b32_e32 v91, 16, v87
	v_mul_f32_e32 v91, 0xbfb8aa3b, v91
	v_mul_f32_e32 v78, 0x3f317217, v88
	v_fma_f32 v78, v88, s93, -v78
	v_fmac_f32_e32 v78, 0x3377d1cf, v88
	v_fmac_f32_e32 v78, 0x3f317217, v88
	v_exp_f32_e32 v91, v91
	v_and_b32_e32 v87, 0xffff0000, v87
	v_sub_f32_e32 v88, 1.0, v79
	v_fmac_f32_e32 v79, v89, v88
	v_max_f32_e32 v79, 0xda24260, v79
	v_sub_f32_e32 v105, 1.0, v79
	v_mov_b32_e32 v88, v79
	v_lshlrev_b32_e32 v79, 16, v86
	v_log_f32_e32 v88, v88
	v_mul_f32_e32 v79, 0xbfb8aa3b, v79
	v_exp_f32_e32 v79, v79
	v_mov_b32_e32 v89, v78
	v_mul_f32_e32 v78, 0x3f317217, v88
	v_fma_f32 v78, v88, s93, -v78
	v_add_f32_e32 v79, 1.0, v79
	v_fmac_f32_e32 v78, 0x3377d1cf, v88
	v_rcp_f32_e32 v79, v79
	v_fmac_f32_e32 v78, 0x3f317217, v88
	v_and_b32_e32 v86, 0xffff0000, v86
	v_mul_f32_e32 v86, 0xbfb8aa3b, v86
	v_mov_b32_e32 v88, v78
	v_sub_f32_e32 v78, 1.0, v72
	v_fma_f32 v72, v79, v78, v72
	v_max_f32_e32 v72, 0xda24260, v72
	v_cmp_gt_f32_e32 vcc, s92, v72
	v_exp_f32_e32 v86, v86
	v_add_f32_e32 v91, 1.0, v91
	v_cndmask_b32_e64 v78, 0, 32, vcc
	v_ldexp_f32 v78, v72, v78
	v_log_f32_e32 v79, v78
	v_sub_f32_e32 v78, 1.0, v72
	v_add_f32_e32 v86, 1.0, v86
	v_rcp_f32_e32 v86, v86
	v_mul_f32_e32 v72, 0x3f317217, v79
	v_fma_f32 v72, v79, s93, -v72
	v_fmac_f32_e32 v72, 0x3377d1cf, v79
	v_fmac_f32_e32 v72, 0x3f317217, v79
	v_cmp_lt_f32_e64 s[48:49], |v79|, s90
	v_rcp_f32_e32 v91, v91
	v_mul_f32_e32 v87, 0xbfb8aa3b, v87
	v_cndmask_b32_e64 v72, v79, v72, s[48:49]
	v_sub_f32_e32 v79, 1.0, v73
	v_fma_f32 v73, v86, v79, v73
	v_max_f32_e32 v73, 0xda24260, v73
	v_cmp_gt_f32_e64 s[48:49], s92, v73
	v_exp_f32_e32 v87, v87
	v_add_f32_e32 v92, 1.0, v92
	v_cndmask_b32_e64 v79, 0, 32, s[48:49]
	v_ldexp_f32 v79, v73, v79
	v_log_f32_e32 v86, v79
	v_cndmask_b32_e32 v79, 0, v179, vcc
	v_sub_f32_e32 v72, v72, v79
	v_sub_f32_e32 v79, 1.0, v73
	v_mul_f32_e32 v73, 0x3f317217, v86
	v_fma_f32 v73, v86, s93, -v73
	v_fmac_f32_e32 v73, 0x3377d1cf, v86
	v_fmac_f32_e32 v73, 0x3f317217, v86
	v_cmp_lt_f32_e64 vcc, |v86|, s90
	v_add_f32_e32 v87, 1.0, v87
	v_rcp_f32_e32 v87, v87
	v_cndmask_b32_e32 v73, v86, v73, vcc
	v_sub_f32_e32 v86, 1.0, v74
; #define LAS __attribute__((address_space(3)))
; __device__ __forceinline__ float sigmoidf_(float x) { return __builtin_amdgcn_rcpf(1.0f + __expf(-x)); }
; template <int CTRL> __device__ __forceinline__ float dpp_add0(float x) { return x + dppf<CTRL>(0.0f, x); }
; template <bool WITHO, bool RAW = false>
; __device__ __forceinline__ void hg_pass(const Frame& F, const bf16_t* P, const float* lbh, int b, int h, int nb, int dir, f32x4 (&S)[4][4], float (&Gsum)[16],
;                                         LAS bf16_t* Vl, LAS bf16_t* Kl, float* OF, const float* ngp) {
;     ...
;         for (int m = 0; m < 4; ++m) { const float z0 = __uint_as_float(zr[m].x << 16), z1 = __uint_as_float(zr[m].x & 0xffff0000u), z2 = __uint_as_float(zr[m].y << 16), z3 = __uint_as_float(zr[m].y & 0xffff0000u);
;             const float zz[4] = {z0, z1, z2, z3};
;             const f32x4 lb4 = *(const f32x4*)(lbh + 16 * m + 4 * g);
; #pragma unroll
;             for (int i = 0; i < 4; ++i) { const float lb = lb4[i]; const float f = fmaxf(lb + (1.0f - lb) * sigmoidf_(zz[i]), 1e-30f); kk[m * 4 + i] = 1.0f - f; c[m * 4 + i] = __logf(f); }
;             *(LAS u32x2*)(Vl + tau * 64 + 16 * m + 4 * g) = vr[m];
;  }
;         if (ci + 1 < HG_U / 16) { const int pos = (ci + 1) * 16 + tau, t = dir ? (HG_U - 1 - pos) : pos; const bf16_t* pr = P + (size_t)hg_row(b, nb, t) * 4096 + h * 64 + 4 * g;
; #pragma unroll
;             for (int m = 0; m < 4; ++m) { zr[m] = *(const u32x2*)(pr + (dir ? 2560 : 2048) + 16 * m); vr[m] = *(const u32x2*)(pr + 3072 + 16 * m); } }
;         float G[16];
; #pragma unroll
;         for (int q = 0; q < 16; ++q) G[q] = c[q];
; #pragma unroll
;         for (int q = 0; q < 16; q += 4) ROW_ALLREDUCE4(G[q], G[q + 1], G[q + 2], G[q + 3]);
; #pragma unroll
;         for (int q = 0; q < 16; ++q) { c[q] = dpp_add0<0x111>(c[q]); c[q] = dpp_add0<0x112>(c[q]); c[q] = dpp_add0<0x114>(c[q]); c[q] = dpp_add0<0x118>(c[q]); }
	v_fma_f32 v74, v91, v86, v74
	v_max_f32_e32 v74, 0xda24260, v74
	v_cndmask_b32_e64 v91, 0, v179, s[48:49]
	v_sub_f32_e32 v73, v73, v91
	v_log_f32_e32 v86, v74
	v_rcp_f32_e32 v92, v92
	v_and_b32_e32 v84, 0xffff0000, v84
	v_mul_f32_e32 v84, 0xbfb8aa3b, v84
	v_mul_f32_e32 v91, 0x3f317217, v86
	v_fma_f32 v91, v86, s93, -v91
	v_fmac_f32_e32 v91, 0x3377d1cf, v86
	v_fmac_f32_e32 v91, 0x3f317217, v86
	v_exp_f32_e32 v84, v84
	v_add_f32_dpp v3, v3, v3 row_shr:2 row_mask:0xf bank_mask:0xf bound_ctrl:1
	v_mov_b32_e32 v86, v91
	v_sub_f32_e32 v91, 1.0, v75
	v_fmac_f32_e32 v75, v87, v91
	v_max_f32_e32 v75, 0xda24260, v75
	v_log_f32_e32 v87, v75
	v_add_f32_e32 v84, 1.0, v84
	v_rcp_f32_e32 v84, v84
	v_add_f32_dpp v3, v3, v3 row_shr:4 row_mask:0xf bank_mask:0xf bound_ctrl:1
	v_mul_f32_e32 v91, 0x3f317217, v87
	v_fma_f32 v91, v87, s93, -v91
	v_fmac_f32_e32 v91, 0x3377d1cf, v87
	v_fmac_f32_e32 v91, 0x3f317217, v87
	v_add_f32_dpp v244, v3, v3 row_shr:8 row_mask:0xf bank_mask:0xf bound_ctrl:1
	v_add_f32_dpp v3, v80, v80 row_shr:1 row_mask:0xf bank_mask:0xf bound_ctrl:1
	v_mov_b32_e32 v87, v91
	v_sub_f32_e32 v91, 1.0, v68
	v_fma_f32 v68, v92, v91, v68
	v_max_f32_e32 v68, 0xda24260, v68
	v_sub_f32_e32 v229, 1.0, v68
	v_add_f32_dpp v3, v3, v3 row_shr:2 row_mask:0xf bank_mask:0xf bound_ctrl:1
	v_log_f32_e32 v91, v68
	v_lshlrev_b32_e32 v92, 16, v85
	v_add_f32_dpp v3, v3, v3 row_shr:4 row_mask:0xf bank_mask:0xf bound_ctrl:1
	v_and_b32_e32 v85, 0xffff0000, v85
	v_mul_f32_e32 v68, 0x3f317217, v91
	v_fma_f32 v68, v91, s93, -v68
	v_fmac_f32_e32 v68, 0x3377d1cf, v91
	v_fmac_f32_e32 v68, 0x3f317217, v91
	v_add_f32_dpp v243, v3, v3 row_shr:8 row_mask:0xf bank_mask:0xf bound_ctrl:1
	v_add_f32_dpp v3, v81, v81 row_shr:1 row_mask:0xf bank_mask:0xf bound_ctrl:1
	v_sub_f32_e32 v91, 1.0, v69
	v_fma_f32 v69, v84, v91, v69
	v_max_f32_e32 v69, 0xda24260, v69
	v_mul_f32_e32 v91, 0xbfb8aa3b, v92
	v_log_f32_e32 v84, v69
	v_exp_f32_e32 v91, v91
	v_add_f32_dpp v3, v3, v3 row_shr:2 row_mask:0xf bank_mask:0xf bound_ctrl:1
	v_sub_f32_e32 v230, 1.0, v69
	v_mul_f32_e32 v69, 0x3f317217, v84
	v_add_f32_dpp v3, v3, v3 row_shr:4 row_mask:0xf bank_mask:0xf bound_ctrl:1
	v_add_f32_e32 v91, 1.0, v91
	v_fma_f32 v69, v84, s93, -v69
	v_add_f32_dpp v242, v3, v3 row_shr:8 row_mask:0xf bank_mask:0xf bound_ctrl:1
	v_add_f32_dpp v3, v90, v90 row_shr:1 row_mask:0xf bank_mask:0xf bound_ctrl:1
	v_rcp_f32_e32 v91, v91
	v_fmac_f32_e32 v69, 0x3377d1cf, v84
	v_add_f32_dpp v3, v3, v3 row_shr:2 row_mask:0xf bank_mask:0xf bound_ctrl:1
	v_fmac_f32_e32 v69, 0x3f317217, v84
	s_nop 0
	v_add_f32_dpp v3, v3, v3 row_shr:4 row_mask:0xf bank_mask:0xf bound_ctrl:1
	v_mul_f32_e32 v85, 0xbfb8aa3b, v85
	s_nop 0
	v_add_f32_dpp v241, v3, v3 row_shr:8 row_mask:0xf bank_mask:0xf bound_ctrl:1
	v_add_f32_dpp v3, v76, v76 row_shr:1 row_mask:0xf bank_mask:0xf bound_ctrl:1
	v_sub_f32_e32 v84, 1.0, v70
	v_fma_f32 v70, v91, v84, v70
	v_add_f32_dpp v3, v3, v3 row_shr:2 row_mask:0xf bank_mask:0xf bound_ctrl:1
	v_max_f32_e32 v70, 0xda24260, v70
	s_nop 0
	v_add_f32_dpp v3, v3, v3 row_shr:4 row_mask:0xf bank_mask:0xf bound_ctrl:1
	v_exp_f32_e32 v85, v85
	s_nop 0
	v_add_f32_dpp v109, v3, v3 row_shr:8 row_mask:0xf bank_mask:0xf bound_ctrl:1
	v_add_f32_dpp v3, v77, v77 row_shr:1 row_mask:0xf bank_mask:0xf bound_ctrl:1
	v_log_f32_e32 v84, v70
	s_nop 0
	v_add_f32_dpp v3, v3, v3 row_shr:2 row_mask:0xf bank_mask:0xf bound_ctrl:1
	v_sub_f32_e32 v231, 1.0, v70
	v_add_f32_e32 v85, 1.0, v85
	v_add_f32_dpp v3, v3, v3 row_shr:4 row_mask:0xf bank_mask:0xf bound_ctrl:1
	v_mul_f32_e32 v70, 0x3f317217, v84
	v_fma_f32 v70, v84, s93, -v70
	v_add_f32_dpp v108, v3, v3 row_shr:8 row_mask:0xf bank_mask:0xf bound_ctrl:1
	v_add_f32_dpp v3, v89, v89 row_shr:1 row_mask:0xf bank_mask:0xf bound_ctrl:1
	v_rcp_f32_e32 v85, v85
	v_fmac_f32_e32 v70, 0x3377d1cf, v84
	v_add_f32_dpp v3, v3, v3 row_shr:2 row_mask:0xf bank_mask:0xf bound_ctrl:1
	v_fmac_f32_e32 v70, 0x3f317217, v84
	s_nop 0
	v_add_f32_dpp v3, v3, v3 row_shr:4 row_mask:0xf bank_mask:0xf bound_ctrl:1
	s_nop 1
	v_add_f32_dpp v107, v3, v3 row_shr:8 row_mask:0xf bank_mask:0xf bound_ctrl:1
	v_add_f32_dpp v3, v88, v88 row_shr:1 row_mask:0xf bank_mask:0xf bound_ctrl:1
	v_sub_f32_e32 v84, 1.0, v71
	s_nop 0
	v_add_f32_dpp v3, v3, v3 row_shr:2 row_mask:0xf bank_mask:0xf bound_ctrl:1
	v_fmac_f32_e32 v71, v85, v84
	v_max_f32_e32 v71, 0xda24260, v71
	v_add_f32_dpp v3, v3, v3 row_shr:4 row_mask:0xf bank_mask:0xf bound_ctrl:1
	v_sub_f32_e32 v232, 1.0, v71
	s_nop 0
	v_add_f32_dpp v106, v3, v3 row_shr:8 row_mask:0xf bank_mask:0xf bound_ctrl:1
	v_add_f32_dpp v3, v72, v72 row_shr:1 row_mask:0xf bank_mask:0xf bound_ctrl:1
	s_nop 1
	v_add_f32_dpp v3, v3, v3 row_shr:2 row_mask:0xf bank_mask:0xf bound_ctrl:1
	v_log_f32_e32 v84, v71
	s_nop 0
	v_add_f32_dpp v3, v3, v3 row_shr:4 row_mask:0xf bank_mask:0xf bound_ctrl:1
	v_mul_f32_e32 v71, 0x3f317217, v84
	s_nop 0
	v_add_f32_dpp v240, v3, v3 row_shr:8 row_mask:0xf bank_mask:0xf bound_ctrl:1
	v_add_f32_dpp v3, v73, v73 row_shr:1 row_mask:0xf bank_mask:0xf bound_ctrl:1
	v_fma_f32 v71, v84, s93, -v71
	v_fmac_f32_e32 v71, 0x3377d1cf, v84
	v_add_f32_dpp v3, v3, v3 row_shr:2 row_mask:0xf bank_mask:0xf bound_ctrl:1
	v_fmac_f32_e32 v71, 0x3f317217, v84
	s_nop 0
	v_add_f32_dpp v3, v3, v3 row_shr:4 row_mask:0xf bank_mask:0xf bound_ctrl:1
	v_mov_b32_e32 v225, v90
	s_nop 0
	v_add_f32_dpp v239, v3, v3 row_shr:8 row_mask:0xf bank_mask:0xf bound_ctrl:1
	v_add_f32_dpp v3, v86, v86 row_shr:1 row_mask:0xf bank_mask:0xf bound_ctrl:1
	s_nop 1
	v_add_f32_dpp v3, v3, v3 row_shr:2 row_mask:0xf bank_mask:0xf bound_ctrl:1
	v_mov_b32_e32 v226, v81
	v_mov_b32_e32 v228, v80
	v_add_f32_dpp v3, v3, v3 row_shr:4 row_mask:0xf bank_mask:0xf bound_ctrl:1
; #define LAS __attribute__((address_space(3)))
; __device__ __forceinline__ unsigned cvt_pk_bf16(float lo, float hi) { unsigned r; asm volatile("v_cvt_pk_bf16_f32 %0, %1, %2" : "=v"(r) : "v"(lo), "v"(hi)); return r; }
; template <int CTRL> __device__ __forceinline__ float dpp_add0(float x) { return x + dppf<CTRL>(0.0f, x); }
; template <bool WITHO, bool RAW = false>
; __device__ __forceinline__ void hg_pass(const Frame& F, const bf16_t* P, const float* lbh, int b, int h, int nb, int dir, f32x4 (&S)[4][4], float (&Gsum)[16],
;                                         LAS bf16_t* Vl, LAS bf16_t* Kl, float* OF, const float* ngp) {
;     ...
;         for (int q = 0; q < 16; ++q) G[q] = c[q];
; #pragma unroll
;         for (int q = 0; q < 16; q += 4) ROW_ALLREDUCE4(G[q], G[q + 1], G[q + 2], G[q + 3]);
; #pragma unroll
;         for (int q = 0; q < 16; ++q) { c[q] = dpp_add0<0x111>(c[q]); c[q] = dpp_add0<0x112>(c[q]); c[q] = dpp_add0<0x114>(c[q]); c[q] = dpp_add0<0x118>(c[q]); }
; #pragma unroll
;         for (int q = 0; q < 16; ++q) Gsum[q] += G[q];
; #pragma unroll
;         for (int m = 0; m < 4; ++m) { float kh[4];
; #pragma unroll
;             for (int i = 0; i < 4; ++i) kh[i] = kk[m * 4 + i] * __expf(G[m * 4 + i] - c[m * 4 + i]);
;             u32x2 w; w.x = cvt_pk_bf16(kh[0], kh[1]); w.y = cvt_pk_bf16(kh[2], kh[3]);
;             *(LAS u32x2*)(Kl + tau * 64 + 16 * m + 4 * g) = w; }
	s_nop 1
	v_add_f32_dpp v227, v227, v227 quad_perm:[1,0,3,2] row_mask:0xf bank_mask:0xf
	v_add_f32_dpp v228, v228, v228 quad_perm:[1,0,3,2] row_mask:0xf bank_mask:0xf
	v_add_f32_dpp v226, v226, v226 quad_perm:[1,0,3,2] row_mask:0xf bank_mask:0xf
	v_add_f32_dpp v225, v225, v225 quad_perm:[1,0,3,2] row_mask:0xf bank_mask:0xf
	v_add_f32_dpp v227, v227, v227 quad_perm:[2,3,0,1] row_mask:0xf bank_mask:0xf
	v_add_f32_dpp v228, v228, v228 quad_perm:[2,3,0,1] row_mask:0xf bank_mask:0xf
	v_add_f32_dpp v226, v226, v226 quad_perm:[2,3,0,1] row_mask:0xf bank_mask:0xf
	v_add_f32_dpp v225, v225, v225 quad_perm:[2,3,0,1] row_mask:0xf bank_mask:0xf
	v_add_f32_dpp v227, v227, v227 row_half_mirror row_mask:0xf bank_mask:0xf
	v_add_f32_dpp v228, v228, v228 row_half_mirror row_mask:0xf bank_mask:0xf
	v_add_f32_dpp v226, v226, v226 row_half_mirror row_mask:0xf bank_mask:0xf
	v_add_f32_dpp v225, v225, v225 row_half_mirror row_mask:0xf bank_mask:0xf
	v_add_f32_dpp v227, v227, v227 row_mirror row_mask:0xf bank_mask:0xf
	v_add_f32_dpp v228, v228, v228 row_mirror row_mask:0xf bank_mask:0xf
	v_add_f32_dpp v226, v226, v226 row_mirror row_mask:0xf bank_mask:0xf
	v_add_f32_dpp v225, v225, v225 row_mirror row_mask:0xf bank_mask:0xf
	v_mov_b32_e32 v215, v68
	v_mov_b32_e32 v216, v69
	v_add_f32_dpp v238, v3, v3 row_shr:8 row_mask:0xf bank_mask:0xf bound_ctrl:1
	v_add_f32_dpp v3, v87, v87 row_shr:1 row_mask:0xf bank_mask:0xf bound_ctrl:1
	v_mov_b32_e32 v213, v70
	v_mov_b32_e32 v221, v89
	v_add_f32_dpp v3, v3, v3 row_shr:2 row_mask:0xf bank_mask:0xf bound_ctrl:1
	v_mov_b32_e32 v223, v77
	v_mov_b32_e32 v222, v88
	v_add_f32_dpp v3, v3, v3 row_shr:4 row_mask:0xf bank_mask:0xf bound_ctrl:1
	v_mov_b32_e32 v224, v76
	v_mov_b32_e32 v218, v73
	v_add_f32_dpp v237, v3, v3 row_shr:8 row_mask:0xf bank_mask:0xf bound_ctrl:1
	v_add_f32_dpp v3, v68, v68 row_shr:1 row_mask:0xf bank_mask:0xf bound_ctrl:1
	v_sub_f32_e32 v68, v228, v243
	v_mul_f32_e32 v68, 0x3fb8aa3b, v68
	v_add_f32_dpp v3, v3, v3 row_shr:2 row_mask:0xf bank_mask:0xf bound_ctrl:1
	v_exp_f32_e32 v68, v68
	v_mov_b32_e32 v217, v87
	v_add_f32_dpp v3, v3, v3 row_shr:4 row_mask:0xf bank_mask:0xf bound_ctrl:1
	v_mov_b32_e32 v220, v72
	v_mov_b32_e32 v219, v86
	v_add_f32_dpp v236, v3, v3 row_shr:8 row_mask:0xf bank_mask:0xf bound_ctrl:1
	v_add_f32_dpp v3, v69, v69 row_shr:1 row_mask:0xf bank_mask:0xf bound_ctrl:1
	v_sub_f32_e32 v69, v226, v242
	v_mul_f32_e32 v69, 0x3fb8aa3b, v69
	v_add_f32_dpp v3, v3, v3 row_shr:2 row_mask:0xf bank_mask:0xf bound_ctrl:1
	v_exp_f32_e32 v69, v69
	v_mov_b32_e32 v214, v71
	v_add_f32_dpp v3, v3, v3 row_shr:4 row_mask:0xf bank_mask:0xf bound_ctrl:1
	v_mul_f32_e32 v68, v101, v68
	v_sub_f32_e32 v83, 1.0, v83
	v_add_f32_dpp v235, v3, v3 row_shr:8 row_mask:0xf bank_mask:0xf bound_ctrl:1
	v_add_f32_dpp v3, v70, v70 row_shr:1 row_mask:0xf bank_mask:0xf bound_ctrl:1
	v_sub_f32_e32 v70, v225, v241
	v_mul_f32_e32 v70, 0x3fb8aa3b, v70
	v_add_f32_dpp v3, v3, v3 row_shr:2 row_mask:0xf bank_mask:0xf bound_ctrl:1
	v_exp_f32_e32 v70, v70
	s_nop 1
	v_add_f32_dpp v224, v224, v224 quad_perm:[1,0,3,2] row_mask:0xf bank_mask:0xf
	v_add_f32_dpp v223, v223, v223 quad_perm:[1,0,3,2] row_mask:0xf bank_mask:0xf
	v_add_f32_dpp v221, v221, v221 quad_perm:[1,0,3,2] row_mask:0xf bank_mask:0xf
	v_add_f32_dpp v222, v222, v222 quad_perm:[1,0,3,2] row_mask:0xf bank_mask:0xf
	v_add_f32_dpp v224, v224, v224 quad_perm:[2,3,0,1] row_mask:0xf bank_mask:0xf
	v_add_f32_dpp v223, v223, v223 quad_perm:[2,3,0,1] row_mask:0xf bank_mask:0xf
	v_add_f32_dpp v221, v221, v221 quad_perm:[2,3,0,1] row_mask:0xf bank_mask:0xf
	v_add_f32_dpp v222, v222, v222 quad_perm:[2,3,0,1] row_mask:0xf bank_mask:0xf
	v_add_f32_dpp v224, v224, v224 row_half_mirror row_mask:0xf bank_mask:0xf
	v_add_f32_dpp v223, v223, v223 row_half_mirror row_mask:0xf bank_mask:0xf
	v_add_f32_dpp v221, v221, v221 row_half_mirror row_mask:0xf bank_mask:0xf
	v_add_f32_dpp v222, v222, v222 row_half_mirror row_mask:0xf bank_mask:0xf
	v_add_f32_dpp v224, v224, v224 row_mirror row_mask:0xf bank_mask:0xf
	v_add_f32_dpp v223, v223, v223 row_mirror row_mask:0xf bank_mask:0xf
	v_add_f32_dpp v221, v221, v221 row_mirror row_mask:0xf bank_mask:0xf
	v_add_f32_dpp v222, v222, v222 row_mirror row_mask:0xf bank_mask:0xf
	s_nop 1
	v_add_f32_dpp v220, v220, v220 quad_perm:[1,0,3,2] row_mask:0xf bank_mask:0xf
	v_add_f32_dpp v218, v218, v218 quad_perm:[1,0,3,2] row_mask:0xf bank_mask:0xf
	v_add_f32_dpp v219, v219, v219 quad_perm:[1,0,3,2] row_mask:0xf bank_mask:0xf
	v_add_f32_dpp v217, v217, v217 quad_perm:[1,0,3,2] row_mask:0xf bank_mask:0xf
	v_add_f32_dpp v220, v220, v220 quad_perm:[2,3,0,1] row_mask:0xf bank_mask:0xf
	v_add_f32_dpp v218, v218, v218 quad_perm:[2,3,0,1] row_mask:0xf bank_mask:0xf
	v_add_f32_dpp v219, v219, v219 quad_perm:[2,3,0,1] row_mask:0xf bank_mask:0xf
	v_add_f32_dpp v217, v217, v217 quad_perm:[2,3,0,1] row_mask:0xf bank_mask:0xf
	v_add_f32_dpp v220, v220, v220 row_half_mirror row_mask:0xf bank_mask:0xf
	v_add_f32_dpp v218, v218, v218 row_half_mirror row_mask:0xf bank_mask:0xf
	v_add_f32_dpp v219, v219, v219 row_half_mirror row_mask:0xf bank_mask:0xf
	v_add_f32_dpp v217, v217, v217 row_half_mirror row_mask:0xf bank_mask:0xf
	v_add_f32_dpp v220, v220, v220 row_mirror row_mask:0xf bank_mask:0xf
	v_add_f32_dpp v218, v218, v218 row_mirror row_mask:0xf bank_mask:0xf
	v_add_f32_dpp v219, v219, v219 row_mirror row_mask:0xf bank_mask:0xf
	v_add_f32_dpp v217, v217, v217 row_mirror row_mask:0xf bank_mask:0xf
	s_nop 1
	v_add_f32_dpp v215, v215, v215 quad_perm:[1,0,3,2] row_mask:0xf bank_mask:0xf
	v_add_f32_dpp v216, v216, v216 quad_perm:[1,0,3,2] row_mask:0xf bank_mask:0xf
; #define LAS __attribute__((address_space(3)))
; __device__ __forceinline__ unsigned cvt_pk_bf16(float lo, float hi) { unsigned r; asm volatile("v_cvt_pk_bf16_f32 %0, %1, %2" : "=v"(r) : "v"(lo), "v"(hi)); return r; }
; template <int CTRL> __device__ __forceinline__ float dpp_add0(float x) { return x + dppf<CTRL>(0.0f, x); }
; template <bool WITHO, bool RAW = false>
; __device__ __forceinline__ void hg_pass(const Frame& F, const bf16_t* P, const float* lbh, int b, int h, int nb, int dir, f32x4 (&S)[4][4], float (&Gsum)[16],
;                                         LAS bf16_t* Vl, LAS bf16_t* Kl, float* OF, const float* ngp) {
;     ...
;         for (int q = 0; q < 16; q += 4) ROW_ALLREDUCE4(G[q], G[q + 1], G[q + 2], G[q + 3]);
; #pragma unroll
;         for (int q = 0; q < 16; ++q) { c[q] = dpp_add0<0x111>(c[q]); c[q] = dpp_add0<0x112>(c[q]); c[q] = dpp_add0<0x114>(c[q]); c[q] = dpp_add0<0x118>(c[q]); }
; #pragma unroll
;         for (int q = 0; q < 16; ++q) Gsum[q] += G[q];
; #pragma unroll
;         for (int m = 0; m < 4; ++m) { float kh[4];
; #pragma unroll
;             for (int i = 0; i < 4; ++i) kh[i] = kk[m * 4 + i] * __expf(G[m * 4 + i] - c[m * 4 + i]);
;             u32x2 w; w.x = cvt_pk_bf16(kh[0], kh[1]); w.y = cvt_pk_bf16(kh[2], kh[3]);
;             *(LAS u32x2*)(Kl + tau * 64 + 16 * m + 4 * g) = w; }
;         float ofv[4][4], gtv[4][4]; int orow[4];
;         if (WITHO) {
; #pragma unroll
;             for (int i = 0; i < 4; ++i) { const int p2 = ci * 16 + 4 * g + i, t2 = dir ? (HG_U - 1 - p2) : p2; orow[i] = hg_row(b, nb, t2); }
	v_add_f32_dpp v213, v213, v213 quad_perm:[1,0,3,2] row_mask:0xf bank_mask:0xf
	v_add_f32_dpp v214, v214, v214 quad_perm:[1,0,3,2] row_mask:0xf bank_mask:0xf
	v_add_f32_dpp v215, v215, v215 quad_perm:[2,3,0,1] row_mask:0xf bank_mask:0xf
	v_add_f32_dpp v216, v216, v216 quad_perm:[2,3,0,1] row_mask:0xf bank_mask:0xf
	v_add_f32_dpp v213, v213, v213 quad_perm:[2,3,0,1] row_mask:0xf bank_mask:0xf
	v_add_f32_dpp v214, v214, v214 quad_perm:[2,3,0,1] row_mask:0xf bank_mask:0xf
	v_add_f32_dpp v215, v215, v215 row_half_mirror row_mask:0xf bank_mask:0xf
	v_add_f32_dpp v216, v216, v216 row_half_mirror row_mask:0xf bank_mask:0xf
	v_add_f32_dpp v213, v213, v213 row_half_mirror row_mask:0xf bank_mask:0xf
	v_add_f32_dpp v214, v214, v214 row_half_mirror row_mask:0xf bank_mask:0xf
	v_add_f32_dpp v215, v215, v215 row_mirror row_mask:0xf bank_mask:0xf
	v_add_f32_dpp v216, v216, v216 row_mirror row_mask:0xf bank_mask:0xf
	v_add_f32_dpp v213, v213, v213 row_mirror row_mask:0xf bank_mask:0xf
	v_add_f32_dpp v214, v214, v214 row_mirror row_mask:0xf bank_mask:0xf
	v_mul_f32_e32 v69, v82, v69
	v_add_f32_dpp v3, v3, v3 row_shr:4 row_mask:0xf bank_mask:0xf bound_ctrl:1
	v_mul_f32_e32 v70, v83, v70
	v_sub_f32_e32 v74, 1.0, v74
	v_add_f32_dpp v234, v3, v3 row_shr:8 row_mask:0xf bank_mask:0xf bound_ctrl:1
	v_add_f32_dpp v3, v71, v71 row_shr:1 row_mask:0xf bank_mask:0xf bound_ctrl:1
	v_sub_f32_e32 v75, 1.0, v75
	s_andn2_b64 vcc, exec, s[4:5]
	v_add_f32_dpp v3, v3, v3 row_shr:2 row_mask:0xf bank_mask:0xf bound_ctrl:1
	s_nop 1
	v_add_f32_dpp v3, v3, v3 row_shr:4 row_mask:0xf bank_mask:0xf bound_ctrl:1
	s_nop 1
	v_add_f32_dpp v233, v3, v3 row_shr:8 row_mask:0xf bank_mask:0xf bound_ctrl:1
	v_sub_f32_e32 v3, v227, v244
	v_mul_f32_e32 v3, 0x3fb8aa3b, v3
	v_exp_f32_e32 v3, v3
	s_nop 0
	v_mul_f32_e32 v3, v100, v3
	v_cvt_pk_bf16_f32 v68, v3, v68
	v_cvt_pk_bf16_f32 v69, v69, v70
	ds_write_b64 v191, v[68:69] offset:34816
	v_sub_f32_e32 v68, v223, v108
	v_sub_f32_e32 v3, v224, v109
	v_mul_f32_e32 v68, 0x3fb8aa3b, v68
	v_sub_f32_e32 v69, v221, v107
	v_mul_f32_e32 v3, 0x3fb8aa3b, v3
	v_exp_f32_e32 v68, v68
	v_mul_f32_e32 v69, 0x3fb8aa3b, v69
	v_sub_f32_e32 v70, v222, v106
	v_exp_f32_e32 v3, v3
	v_exp_f32_e32 v69, v69
	v_mul_f32_e32 v70, 0x3fb8aa3b, v70
	v_exp_f32_e32 v70, v70
	v_mul_f32_e32 v68, v103, v68
	v_mul_f32_e32 v3, v102, v3
	v_mul_f32_e32 v69, v104, v69
	v_cvt_pk_bf16_f32 v68, v3, v68
	v_mul_f32_e32 v70, v105, v70
	v_cvt_pk_bf16_f32 v69, v69, v70
	ds_write_b64 v191, v[68:69] offset:34848
	v_sub_f32_e32 v68, v218, v239
	v_sub_f32_e32 v3, v220, v240
	v_mul_f32_e32 v68, 0x3fb8aa3b, v68
	v_sub_f32_e32 v69, v219, v238
	v_mul_f32_e32 v3, 0x3fb8aa3b, v3
	v_exp_f32_e32 v68, v68
	v_mul_f32_e32 v69, 0x3fb8aa3b, v69
	v_sub_f32_e32 v70, v217, v237
	v_exp_f32_e32 v3, v3
	v_exp_f32_e32 v69, v69
	v_mul_f32_e32 v70, 0x3fb8aa3b, v70
	v_exp_f32_e32 v70, v70
	v_mul_f32_e32 v68, v79, v68
	v_mul_f32_e32 v3, v78, v3
	v_mul_f32_e32 v69, v74, v69
	v_cvt_pk_bf16_f32 v68, v3, v68
	v_mul_f32_e32 v70, v75, v70
	v_cvt_pk_bf16_f32 v69, v69, v70
	ds_write_b64 v191, v[68:69] offset:34880
	v_sub_f32_e32 v68, v216, v235
	v_sub_f32_e32 v3, v215, v236
	v_mul_f32_e32 v68, 0x3fb8aa3b, v68
	v_sub_f32_e32 v69, v213, v234
	v_mul_f32_e32 v3, 0x3fb8aa3b, v3
	v_exp_f32_e32 v68, v68
	v_mul_f32_e32 v69, 0x3fb8aa3b, v69
	v_sub_f32_e32 v70, v214, v233
	v_exp_f32_e32 v3, v3
	v_exp_f32_e32 v69, v69
	v_mul_f32_e32 v70, 0x3fb8aa3b, v70
	v_exp_f32_e32 v70, v70
	v_mul_f32_e32 v68, v230, v68
	v_mul_f32_e32 v3, v229, v3
	v_mul_f32_e32 v69, v231, v69
	v_cvt_pk_bf16_f32 v68, v3, v68
	v_mul_f32_e32 v70, v232, v70
	v_cvt_pk_bf16_f32 v69, v69, v70
	ds_write_b64 v191, v[68:69] offset:34912
	v_add_u32_e32 v68, s26, v193
	v_add_u32_e32 v3, s27, v114
	v_add_u32_e32 v69, 0x7f, v68
	v_cndmask_b32_e64 v69, v69, v3, s[0:1]
	v_add_u32_e32 v172, s25, v69
	v_add_u32_e32 v69, 1, v3
	v_add_u32_e32 v70, 0x7e, v68
	v_cndmask_b32_e64 v69, v70, v69, s[0:1]
	v_add_u32_e32 v90, s25, v69
	v_add_u32_e32 v69, 2, v3
	v_add_u32_e32 v70, 0x7d, v68
	v_add_u32_e32 v3, 3, v3
	v_add_u32_e32 v68, 0x7c, v68
	v_cndmask_b32_e64 v69, v70, v69, s[0:1]
	v_cndmask_b32_e64 v3, v68, v3, s[0:1]
	v_add_u32_e32 v86, s25, v69
	v_add_u32_e32 v70, s25, v3
	v_ashrrev_i32_e32 v173, 31, v172
	v_ashrrev_i32_e32 v91, 31, v90
	v_ashrrev_i32_e32 v87, 31, v86
	v_ashrrev_i32_e32 v71, 31, v70
	s_cbranch_vccnz .LBB0_1174
; __device__ __forceinline__ float bf2f(unsigned short b) { return __uint_as_float(((unsigned)b) << 16); }
; __device__ __forceinline__ float siluf_(float x) { return x * sigmoidf_(x); }
; template <bool WITHO, bool RAW = false>
; __device__ __forceinline__ void hg_pass(const Frame& F, const bf16_t* P, const float* lbh, int b, int h, int nb, int dir, f32x4 (&S)[4][4], float (&Gsum)[16],
;                                         LAS bf16_t* Vl, LAS bf16_t* Kl, float* OF, const float* ngp) {
;     ...
;             for (int i = 0; i < 4; ++i) { const int p2 = ci * 16 + 4 * g + i, t2 = dir ? (HG_U - 1 - p2) : p2; orow[i] = hg_row(b, nb, t2); }
;             if (dir && !RAW) {
; #pragma unroll
;                 for (int i = 0; i < 4; ++i)
; #pragma unroll
;                     for (int vt = 0; vt < 4; ++vt) { ofv[i][vt] = OF[(size_t)orow[i] * 512 + h * 64 + 16 * vt + tau]; gtv[i][vt] = bf2f(P[(size_t)orow[i] * 4096 + 3584 + h * 64 + 16 * vt + tau]); }
;     ...
;                     const float qq[4] = {__uint_as_float(qr[m].x << 16), __uint_as_float(qr[m].x & 0xffff0000u), __uint_as_float(qr[m].y << 16), __uint_as_float(qr[m].y & 0xffff0000u)};
; #pragma unroll
;                     for (int i = 0; i < 4; ++i) { const int q = m * 4 + i; const float qv = siluf_(qq[i]) * 0.125f; const float d = fminf(fmaxf(c[q] - 0.5f * G[q], -80.0f), 80.0f);
;                         qt_[mm * 4 + i] = qv * __expf(d); kt_[mm * 4 + i] = kk[q] * __expf(-d); qh_[mm * 4 + i] = qv * __expf(c[q]); } }
	v_lshlrev_b64 v[72:73], 13, v[172:173]
	v_lshl_add_u64 v[72:73], v[132:133], 0, v[72:73]
	v_add_co_u32_e32 v72, vcc, 0x1000, v72
	v_lshlrev_b64 v[80:81], 13, v[90:91]
	s_nop 0
	v_addc_co_u32_e32 v73, vcc, 0, v73, vcc
	v_lshl_add_u64 v[80:81], v[132:133], 0, v[80:81]
	v_lshlrev_b64 v[76:77], 11, v[90:91]
	v_add_co_u32_e32 v80, vcc, s97, v80
	v_lshl_add_u64 v[76:77], v[130:131], 0, v[76:77]
	s_nop 0
	v_addc_co_u32_e32 v81, vcc, 0, v81, vcc
	global_load_dword v197, v[76:77], off
	global_load_dword v198, v[76:77], off offset:64
	global_load_ushort v3, v[80:81], off offset:3104
	global_load_ushort v84, v[80:81], off offset:3168
	global_load_ushort v85, v[80:81], off offset:3136
	global_load_ushort v88, v[80:81], off offset:3072
	global_load_dword v199, v[76:77], off offset:128
	global_load_dword v200, v[76:77], off offset:192
	v_lshlrev_b64 v[80:81], 13, v[86:87]
	v_lshl_add_u64 v[80:81], v[132:133], 0, v[80:81]
	v_lshlrev_b64 v[76:77], 11, v[86:87]
	v_add_co_u32_e32 v80, vcc, s97, v80
	v_lshl_add_u64 v[76:77], v[130:131], 0, v[76:77]
	s_nop 0
	v_addc_co_u32_e32 v81, vcc, 0, v81, vcc
	global_load_dword v201, v[76:77], off
	global_load_dword v202, v[76:77], off offset:64
	global_load_ushort v89, v[80:81], off offset:3104
	global_load_ushort v92, v[80:81], off offset:3136
	global_load_ushort v93, v[80:81], off offset:3168
	global_load_ushort v160, v[80:81], off offset:3072
	global_load_dword v203, v[76:77], off offset:128
	global_load_dword v204, v[76:77], off offset:192
	v_lshlrev_b64 v[80:81], 13, v[70:71]
	v_lshl_add_u64 v[80:81], v[132:133], 0, v[80:81]
	v_lshlrev_b64 v[76:77], 11, v[70:71]
	v_add_co_u32_e32 v80, vcc, s97, v80
	v_lshlrev_b64 v[68:69], 11, v[172:173]
	v_lshl_add_u64 v[76:77], v[130:131], 0, v[76:77]
	v_addc_co_u32_e32 v81, vcc, 0, v81, vcc
	v_lshl_add_u64 v[68:69], v[130:131], 0, v[68:69]
	global_load_dword v205, v[76:77], off
	global_load_dword v206, v[76:77], off offset:64
	global_load_ushort v164, v[80:81], off offset:3072
	global_load_ushort v165, v[80:81], off offset:3104
	global_load_dword v209, v[76:77], off offset:128
	global_load_ushort v170, v[80:81], off offset:3136
	s_nop 0
	global_load_ushort v80, v[80:81], off offset:3168
	s_nop 0
	global_load_dword v212, v[76:77], off offset:192
	s_nop 0
	global_load_ushort v76, v[72:73], off offset:3136
	global_load_ushort v77, v[72:73], off offset:3168
	global_load_ushort v81, v[72:73], off offset:3072
	s_nop 0
	global_load_ushort v72, v[72:73], off offset:3104
	s_nop 0
	global_load_dword v207, v[68:69], off
	global_load_dword v208, v[68:69], off offset:64
	global_load_dword v210, v[68:69], off offset:128
	global_load_dword v211, v[68:69], off offset:192
	s_waitcnt vmcnt(0)
	v_lshlrev_b32_e32 v156, 16, v3
	v_lshlrev_b32_e32 v158, 16, v84
	v_lshlrev_b32_e32 v159, 16, v85
	v_lshlrev_b32_e32 v157, 16, v88
	v_lshlrev_b32_e32 v162, 16, v92
	v_lshlrev_b32_e32 v163, 16, v93
	v_lshlrev_b32_e32 v161, 16, v160
	v_lshlrev_b32_e32 v160, 16, v89
	v_lshlrev_b32_e32 v165, 16, v165
	v_lshlrev_b32_e32 v164, 16, v164
	v_lshlrev_b32_e32 v171, 16, v80
	v_lshlrev_b32_e32 v170, 16, v170
	v_lshlrev_b32_e32 v169, 16, v76
	v_lshlrev_b32_e32 v168, 16, v77
	v_lshlrev_b32_e32 v167, 16, v81
	v_lshlrev_b32_e32 v166, 16, v72
.LBB0_1174:
	s_waitcnt vmcnt(8)
	v_lshlrev_b32_e32 v182, 16, v0
	v_mul_f32_e32 v3, 0xbfb8aa3b, v182
	v_exp_f32_e32 v68, v3
	v_and_b32_e32 v183, 0xffff0000, v0
	v_mul_f32_e32 v247, 0xbfb8aa3b, v183
	v_exp_f32_e32 v247, v247
	v_add_f32_e32 v0, 1.0, v68
	v_rcp_f32_e32 v184, v0
	v_lshlrev_b32_e32 v185, 16, v1
	v_add_f32_e32 v247, 1.0, v247
	v_rcp_f32_e32 v247, v247
	v_mul_f32_e32 v182, v184, v182
	v_fma_f32 v184, -0.5, v227, v244
	v_med3_f32 v184, v184, s94, v180
	v_mul_f32_e32 v246, 0x3fb8aa3b, v184
	v_mul_f32_e32 v184, 0xbfb8aa3b, v184
	v_exp_f32_e32 v184, v184
	v_mul_f32_e32 v244, 0x3fb8aa3b, v244
	v_mul_f32_e32 v183, v247, v183
	v_mul_f32_e32 v247, 0xbfb8aa3b, v185
	v_exp_f32_e32 v246, v246
	v_exp_f32_e32 v244, v244
	v_exp_f32_e32 v247, v247
	v_mul_f32_e32 v100, v100, v184
	v_fma_f32 v184, -0.5, v228, v243
	v_mul_f32_e32 v182, 0x3e000000, v182
	v_med3_f32 v184, v184, s94, v180
	v_mul_f32_e32 v246, v182, v246
	v_mul_f32_e32 v182, v182, v244
	v_mul_f32_e32 v244, 0x3fb8aa3b, v184
	v_mul_f32_e32 v184, 0xbfb8aa3b, v184
	v_add_f32_e32 v247, 1.0, v247
	v_exp_f32_e32 v184, v184
	v_rcp_f32_e32 v247, v247
	v_and_b32_e32 v245, 0xffff0000, v1
	v_mul_f32_e32 v243, 0x3fb8aa3b, v243
	v_exp_f32_e32 v244, v244
	v_exp_f32_e32 v243, v243
	v_mul_f32_e32 v101, v101, v184
	v_mul_f32_e32 v184, v247, v185
	v_mul_f32_e32 v247, 0xbfb8aa3b, v245
	v_exp_f32_e32 v247, v247
	v_fma_f32 v185, -0.5, v226, v242
	v_mul_f32_e32 v183, 0x3e000000, v183
	v_med3_f32 v185, v185, s94, v180
	v_mul_f32_e32 v244, v183, v244
	v_mul_f32_e32 v183, v183, v243
	v_mul_f32_e32 v243, 0x3fb8aa3b, v185
	v_mul_f32_e32 v242, 0x3fb8aa3b, v242
	v_exp_f32_e32 v243, v243
	v_mul_f32_e32 v185, 0xbfb8aa3b, v185
	v_exp_f32_e32 v242, v242
	v_add_f32_e32 v247, 1.0, v247
	v_exp_f32_e32 v185, v185
	v_rcp_f32_e32 v247, v247
	v_mul_f32_e32 v184, 0x3e000000, v184
	v_mul_f32_e32 v243, v184, v243
	v_mul_f32_e32 v184, v184, v242
	v_fma_f32 v242, -0.5, v225, v241
	v_mul_f32_e32 v82, v82, v185
	v_mul_f32_e32 v185, v247, v245
	v_med3_f32 v242, v242, s94, v180
	v_lshlrev_b32_e32 v247, 16, v98
	v_mul_f32_e32 v245, 0x3fb8aa3b, v242
	v_mul_f32_e32 v241, 0x3fb8aa3b, v241
	v_mul_f32_e32 v248, 0xbfb8aa3b, v247
	v_exp_f32_e32 v245, v245
	v_exp_f32_e32 v241, v241
	v_exp_f32_e32 v248, v248
	v_and_b32_e32 v98, 0xffff0000, v98
	v_mul_f32_e32 v185, 0x3e000000, v185
	v_mul_f32_e32 v249, 0xbfb8aa3b, v98
	v_mul_f32_e32 v245, v185, v245
	v_mul_f32_e32 v185, v185, v241
; __device__ __forceinline__ unsigned cvt_pk_bf16(float lo, float hi) { unsigned r; asm volatile("v_cvt_pk_bf16_f32 %0, %1, %2" : "=v"(r) : "v"(lo), "v"(hi)); return r; }
; template <bool WITHO, bool RAW = false>
; __device__ __forceinline__ void hg_pass(const Frame& F, const bf16_t* P, const float* lbh, int b, int h, int nb, int dir, f32x4 (&S)[4][4], float (&Gsum)[16],
;                                         LAS bf16_t* Vl, LAS bf16_t* Kl, float* OF, const float* ngp) {
;     ...
;         asm volatile("s_waitcnt lgkmcnt(0)" ::: "memory");
;         u32x2 vtr[4], ktr[4];
;         asm volatile("ds_read_b64_tr_b16 %0, %8\n\tds_read_b64_tr_b16 %1, %8 offset:32\n\tds_read_b64_tr_b16 %2, %8 offset:64\n\tds_read_b64_tr_b16 %3, %8 offset:96\n\t"
;                      "ds_read_b64_tr_b16 %4, %9\n\tds_read_b64_tr_b16 %5, %9 offset:32\n\tds_read_b64_tr_b16 %6, %9 offset:64\n\tds_read_b64_tr_b16 %7, %9 offset:96\n\ts_waitcnt lgkmcnt(0)"
;                      : "=&v"(vtr[0]), "=&v"(vtr[1]), "=&v"(vtr[2]), "=&v"(vtr[3]), "=&v"(ktr[0]), "=&v"(ktr[1]), "=&v"(ktr[2]), "=&v"(ktr[3]) : "v"(vaddr), "v"(kaddr) : "memory");
;         bf16x8 Vf[4], Kf[4];
; #pragma unroll
;         for (int q = 0; q < 4; ++q) { u32x4 w; w.x = vtr[q].x; w.y = vtr[q].y; w.z = 0u; w.w = 0u; __builtin_memcpy(&Vf[q], &w, 16); u32x4 w2; w2.x = ktr[q].x; w2.y = ktr[q].y; w2.z = 0u; w2.w = 0u; __builtin_memcpy(&Kf[q], &w2, 16); }
;         if (WITHO) {
;             bf16x8 Ktf[2], Qtf[2], Qhf[2];
; #pragma unroll
;             for (int ks = 0; ks < 2; ++ks) { float kt_[8], qt_[8], qh_[8];
; #pragma unroll
;                 for (int mm = 0; mm < 2; ++mm) { const int m = 2 * ks + mm;
;                     const float qq[4] = {__uint_as_float(qr[m].x << 16), __uint_as_float(qr[m].x & 0xffff0000u), __uint_as_float(qr[m].y << 16), __uint_as_float(qr[m].y & 0xffff0000u)};
; #pragma unroll
;                     for (int i = 0; i < 4; ++i) { const int q = m * 4 + i; const float qv = siluf_(qq[i]) * 0.125f; const float d = fminf(fmaxf(c[q] - 0.5f * G[q], -80.0f), 80.0f);
;                         qt_[mm * 4 + i] = qv * __expf(d); kt_[mm * 4 + i] = kk[q] * __expf(-d); qh_[mm * 4 + i] = qv * __expf(c[q]); } }
;                 u32x4 w; w.x = cvt_pk_bf16(kt_[0], kt_[1]); w.y = cvt_pk_bf16(kt_[2], kt_[3]); w.z = cvt_pk_bf16(kt_[4], kt_[5]); w.w = cvt_pk_bf16(kt_[6], kt_[7]); __builtin_memcpy(&Ktf[ks], &w, 16);
	v_add_f32_e32 v241, 1.0, v248
	v_exp_f32_e32 v249, v249
	v_rcp_f32_e32 v241, v241
	v_mul_f32_e32 v242, 0xbfb8aa3b, v242
	v_exp_f32_e32 v242, v242
	v_add_f32_e32 v249, 1.0, v249
	v_mul_f32_e32 v241, v241, v247
	v_fma_f32 v247, -0.5, v224, v109
	v_rcp_f32_e32 v249, v249
	v_med3_f32 v247, v247, s94, v180
	v_mul_f32_e32 v248, 0x3fb8aa3b, v247
	v_mul_f32_e32 v109, 0x3fb8aa3b, v109
	v_mul_f32_e32 v83, v83, v242
	v_lshlrev_b32_e32 v242, 16, v99
	v_exp_f32_e32 v248, v248
	v_exp_f32_e32 v109, v109
	v_mul_f32_e32 v247, 0xbfb8aa3b, v247
	v_mul_f32_e32 v98, v249, v98
	v_mul_f32_e32 v249, 0xbfb8aa3b, v242
	v_exp_f32_e32 v247, v247
	v_exp_f32_e32 v249, v249
	v_mul_f32_e32 v241, 0x3e000000, v241
	v_mul_f32_e32 v248, v241, v248
	v_mul_f32_e32 v109, v241, v109
	v_fma_f32 v241, -0.5, v223, v108
	v_med3_f32 v241, v241, s94, v180
	v_mul_f32_e32 v102, v102, v247
	v_mul_f32_e32 v247, 0x3fb8aa3b, v241
	v_mul_f32_e32 v108, 0x3fb8aa3b, v108
	v_add_f32_e32 v249, 1.0, v249
	v_exp_f32_e32 v247, v247
	v_exp_f32_e32 v108, v108
	v_rcp_f32_e32 v249, v249
	v_mul_f32_e32 v241, 0xbfb8aa3b, v241
	v_and_b32_e32 v99, 0xffff0000, v99
	v_mul_f32_e32 v98, 0x3e000000, v98
	v_exp_f32_e32 v241, v241
	v_mul_f32_e32 v247, v98, v247
	v_mul_f32_e32 v108, v98, v108
	v_mul_f32_e32 v98, v249, v242
	v_mul_f32_e32 v249, 0xbfb8aa3b, v99
	v_exp_f32_e32 v249, v249
	v_mul_f32_e32 v103, v103, v241
	v_fma_f32 v241, -0.5, v221, v107
	v_med3_f32 v241, v241, s94, v180
	v_mul_f32_e32 v242, 0x3fb8aa3b, v241
	v_mul_f32_e32 v241, 0xbfb8aa3b, v241
	v_mul_f32_e32 v107, 0x3fb8aa3b, v107
	v_add_f32_e32 v249, 1.0, v249
	v_exp_f32_e32 v242, v242
	v_exp_f32_e32 v241, v241
	v_exp_f32_e32 v107, v107
	v_rcp_f32_e32 v249, v249
	v_mul_f32_e32 v98, 0x3e000000, v98
	v_mul_f32_e32 v242, v98, v242
	v_mul_f32_e32 v104, v104, v241
	v_mul_f32_e32 v241, v98, v107
	v_mul_f32_e32 v98, v249, v99
	v_fma_f32 v99, -0.5, v222, v106
	v_med3_f32 v99, v99, s94, v180
	v_mul_f32_e32 v107, 0x3fb8aa3b, v99
	v_mul_f32_e32 v99, 0xbfb8aa3b, v99
	v_mul_f32_e32 v106, 0x3fb8aa3b, v106
	v_exp_f32_e32 v107, v107
	v_exp_f32_e32 v99, v99
	v_exp_f32_e32 v106, v106
	s_waitcnt lgkmcnt(0)
	v_mul_f32_e32 v98, 0x3e000000, v98
	ds_read_b64_tr_b16 v[0:1], v113
	ds_read_b64_tr_b16 v[80:81], v113 offset:32
	ds_read_b64_tr_b16 v[76:77], v113 offset:64
	ds_read_b64_tr_b16 v[72:73], v113 offset:96
	ds_read_b64_tr_b16 v[92:93], v145
	ds_read_b64_tr_b16 v[88:89], v145 offset:32
	ds_read_b64_tr_b16 v[84:85], v145 offset:64
	ds_read_b64_tr_b16 v[68:69], v145 offset:96
	s_waitcnt lgkmcnt(0)
	v_mul_f32_e32 v107, v98, v107
	v_mul_f32_e32 v105, v105, v99
	v_mul_f32_e32 v249, v98, v106
	v_cvt_pk_bf16_f32 v98, v100, v101
	v_cvt_pk_bf16_f32 v99, v82, v83
	v_lshlrev_b32_e32 v82, 16, v96
	v_mul_f32_e32 v83, 0xbfb8aa3b, v82
	v_exp_f32_e32 v83, v83
	v_and_b32_e32 v96, 0xffff0000, v96
	v_cvt_pk_bf16_f32 v100, v102, v103
	v_cvt_pk_bf16_f32 v101, v104, v105
	v_add_f32_e32 v83, 1.0, v83
	v_rcp_f32_e32 v83, v83
	v_cvt_pk_bf16_f32 v102, v246, v244
	v_cvt_pk_bf16_f32 v103, v243, v245
	v_cvt_pk_bf16_f32 v104, v248, v247
	v_cvt_pk_bf16_f32 v105, v242, v107
	v_cvt_pk_bf16_f32 v106, v182, v183
	v_cvt_pk_bf16_f32 v107, v184, v185
	v_mul_f32_e32 v184, 0xbfb8aa3b, v96
	v_exp_f32_e32 v184, v184
	v_mul_f32_e32 v82, v83, v82
	v_fma_f32 v83, -0.5, v220, v240
	v_med3_f32 v83, v83, s94, v180
	v_mul_f32_e32 v183, 0x3fb8aa3b, v83
	v_mul_f32_e32 v83, 0xbfb8aa3b, v83
	v_mul_f32_e32 v185, 0x3fb8aa3b, v240
	v_add_f32_e32 v184, 1.0, v184
	v_exp_f32_e32 v183, v183
	v_exp_f32_e32 v83, v83
	v_exp_f32_e32 v185, v185
	v_rcp_f32_e32 v184, v184
	v_lshlrev_b32_e32 v182, 16, v97
	v_mul_f32_e32 v82, 0x3e000000, v82
	v_mul_f32_e32 v183, v82, v183
	v_mul_f32_e32 v78, v78, v83
	v_mul_f32_e32 v82, v82, v185
	v_mul_f32_e32 v83, v184, v96
	v_fma_f32 v96, -0.5, v218, v239
	v_mul_f32_e32 v185, 0xbfb8aa3b, v182
	v_med3_f32 v96, v96, s94, v180
	v_exp_f32_e32 v185, v185
	v_mul_f32_e32 v184, 0x3fb8aa3b, v96
	v_mul_f32_e32 v239, 0x3fb8aa3b, v239
	v_exp_f32_e32 v184, v184
	v_exp_f32_e32 v239, v239
	v_mul_f32_e32 v96, 0xbfb8aa3b, v96
	v_add_f32_e32 v185, 1.0, v185
	v_and_b32_e32 v97, 0xffff0000, v97
	v_mul_f32_e32 v83, 0x3e000000, v83
	v_exp_f32_e32 v96, v96
	v_rcp_f32_e32 v185, v185
	v_mul_f32_e32 v184, v83, v184
	v_mul_f32_e32 v83, v83, v239
	v_mul_f32_e32 v239, 0xbfb8aa3b, v97
	v_exp_f32_e32 v239, v239
	v_mul_f32_e32 v79, v79, v96
	v_mul_f32_e32 v96, v185, v182
	v_fma_f32 v182, -0.5, v219, v238
	v_med3_f32 v182, v182, s94, v180
	v_mul_f32_e32 v185, 0x3fb8aa3b, v182
	v_mul_f32_e32 v182, 0xbfb8aa3b, v182
	v_mul_f32_e32 v238, 0x3fb8aa3b, v238
	v_add_f32_e32 v239, 1.0, v239
	v_exp_f32_e32 v185, v185
	v_exp_f32_e32 v182, v182
	v_exp_f32_e32 v238, v238
	v_rcp_f32_e32 v239, v239
	v_mul_f32_e32 v96, 0x3e000000, v96
	v_mul_f32_e32 v185, v96, v185
	v_mul_f32_e32 v74, v74, v182
	v_mul_f32_e32 v182, v96, v238
	v_mul_f32_e32 v96, v239, v97
	v_fma_f32 v97, -0.5, v217, v237
	v_med3_f32 v97, v97, s94, v180
	v_lshlrev_b32_e32 v239, 16, v94
	v_mul_f32_e32 v238, 0x3fb8aa3b, v97
	v_mul_f32_e32 v237, 0x3fb8aa3b, v237
	v_mul_f32_e32 v240, 0xbfb8aa3b, v239
	v_exp_f32_e32 v238, v238
	v_exp_f32_e32 v237, v237
	v_exp_f32_e32 v240, v240
	v_mul_f32_e32 v96, 0x3e000000, v96
	v_and_b32_e32 v94, 0xffff0000, v94
	v_cvt_pk_bf16_f32 v108, v109, v108
	v_cvt_pk_bf16_f32 v109, v241, v249
	v_mul_f32_e32 v238, v96, v238
	v_mul_f32_e32 v237, v96, v237
	v_add_f32_e32 v96, 1.0, v240
	v_mul_f32_e32 v241, 0xbfb8aa3b, v94
	v_rcp_f32_e32 v96, v96
	v_exp_f32_e32 v241, v241
	v_mul_f32_e32 v97, 0xbfb8aa3b, v97
	v_exp_f32_e32 v97, v97
	v_mul_f32_e32 v96, v96, v239
	v_fma_f32 v239, -0.5, v215, v236
	v_add_f32_e32 v241, 1.0, v241
	v_med3_f32 v239, v239, s94, v180
; __device__ __forceinline__ float siluf_(float x) { return x * sigmoidf_(x); }
; template <bool WITHO, bool RAW = false>
; __device__ __forceinline__ void hg_pass(const Frame& F, const bf16_t* P, const float* lbh, int b, int h, int nb, int dir, f32x4 (&S)[4][4], float (&Gsum)[16],
;                                         LAS bf16_t* Vl, LAS bf16_t* Kl, float* OF, const float* ngp) {
;     ...
;             for (int ks = 0; ks < 2; ++ks) { float kt_[8], qt_[8], qh_[8];
; #pragma unroll
;                 for (int mm = 0; mm < 2; ++mm) { const int m = 2 * ks + mm;
;                     const float qq[4] = {__uint_as_float(qr[m].x << 16), __uint_as_float(qr[m].x & 0xffff0000u), __uint_as_float(qr[m].y << 16), __uint_as_float(qr[m].y & 0xffff0000u)};
; #pragma unroll
;                     for (int i = 0; i < 4; ++i) { const int q = m * 4 + i; const float qv = siluf_(qq[i]) * 0.125f; const float d = fminf(fmaxf(c[q] - 0.5f * G[q], -80.0f), 80.0f);
;                         qt_[mm * 4 + i] = qv * __expf(d); kt_[mm * 4 + i] = kk[q] * __expf(-d); qh_[mm * 4 + i] = qv * __expf(c[q]); } }
;                 u32x4 w; w.x = cvt_pk_bf16(kt_[0], kt_[1]); w.y = cvt_pk_bf16(kt_[2], kt_[3]); w.z = cvt_pk_bf16(kt_[4], kt_[5]); w.w = cvt_pk_bf16(kt_[6], kt_[7]); __builtin_memcpy(&Ktf[ks], &w, 16);
;                 w.x = cvt_pk_bf16(qt_[0], qt_[1]); w.y = cvt_pk_bf16(qt_[2], qt_[3]); w.z = cvt_pk_bf16(qt_[4], qt_[5]); w.w = cvt_pk_bf16(qt_[6], qt_[7]); __builtin_memcpy(&Qtf[ks], &w, 16);
;                 w.x = cvt_pk_bf16(qh_[0], qh_[1]); w.y = cvt_pk_bf16(qh_[2], qh_[3]); w.z = cvt_pk_bf16(qh_[4], qh_[5]); w.w = cvt_pk_bf16(qh_[6], qh_[7]); __builtin_memcpy(&Qhf[ks], &w, 16); }
;             f32x4 AT = (f32x4){0.f, 0.f, 0.f, 0.f};
;             AT = __builtin_amdgcn_mfma_f32_16x16x32_bf16(Ktf[0], Qtf[0], AT, 0, 0, 0); AT = __builtin_amdgcn_mfma_f32_16x16x32_bf16(Ktf[1], Qtf[1], AT, 0, 0, 0);
; #pragma unroll
;             for (int i = 0; i < 4; ++i) AT[i] = (4 * g + i <= tau) ? AT[i] : 0.0f;
;             bf16x8 Af; { u32x4 w; w.x = cvt_pk_bf16(AT[0], AT[1]); w.y = cvt_pk_bf16(AT[2], AT[3]); w.z = 0u; w.w = 0u; __builtin_memcpy(&Af, &w, 16); }
;             f32x4 o[4];
; #pragma unroll
;             for (int vt = 0; vt < 4; ++vt) { o[vt] = __builtin_amdgcn_mfma_f32_16x16x32_bf16(Af, Vf[vt], (f32x4){0.f, 0.f, 0.f, 0.f}, 0, 0, 0);
; #pragma unroll
	v_rcp_f32_e32 v241, v241
	v_mul_f32_e32 v240, 0x3fb8aa3b, v239
	v_mul_f32_e32 v236, 0x3fb8aa3b, v236
	v_exp_f32_e32 v240, v240
	v_exp_f32_e32 v236, v236
	v_mul_f32_e32 v75, v75, v97
	v_lshlrev_b32_e32 v97, 16, v95
	v_mul_f32_e32 v239, 0xbfb8aa3b, v239
	v_mul_f32_e32 v94, v241, v94
	v_mul_f32_e32 v241, 0xbfb8aa3b, v97
	v_mul_f32_e32 v96, 0x3e000000, v96
	v_exp_f32_e32 v239, v239
	v_exp_f32_e32 v241, v241
	v_mul_f32_e32 v240, v96, v240
	v_mul_f32_e32 v236, v96, v236
	v_fma_f32 v96, -0.5, v216, v235
	v_mul_f32_e32 v235, 0x3fb8aa3b, v235
	v_exp_f32_e32 v235, v235
	v_med3_f32 v96, v96, s94, v180
	v_mul_f32_e32 v229, v229, v239
	v_mul_f32_e32 v239, 0x3fb8aa3b, v96
	v_add_f32_e32 v241, 1.0, v241
	v_and_b32_e32 v95, 0xffff0000, v95
	v_mul_f32_e32 v94, 0x3e000000, v94
	v_exp_f32_e32 v239, v239
	v_rcp_f32_e32 v241, v241
	v_mul_f32_e32 v96, 0xbfb8aa3b, v96
	v_mul_f32_e32 v242, v94, v235
	v_mul_f32_e32 v235, 0xbfb8aa3b, v95
	v_exp_f32_e32 v96, v96
	v_exp_f32_e32 v235, v235
	v_mul_f32_e32 v239, v94, v239
	v_mul_f32_e32 v94, v241, v97
	v_fma_f32 v97, -0.5, v213, v234
	v_med3_f32 v97, v97, s94, v180
	v_mul_f32_e32 v96, v230, v96
	v_mul_f32_e32 v230, 0x3fb8aa3b, v97
	v_mul_f32_e32 v234, 0x3fb8aa3b, v234
	v_add_f32_e32 v235, 1.0, v235
	v_exp_f32_e32 v230, v230
	v_exp_f32_e32 v234, v234
	v_rcp_f32_e32 v235, v235
	v_mul_f32_e32 v97, 0xbfb8aa3b, v97
	v_mul_f32_e32 v94, 0x3e000000, v94
	v_exp_f32_e32 v97, v97
	v_mul_f32_e32 v241, v94, v230
	v_mul_f32_e32 v243, v94, v234
	v_mul_f32_e32 v94, v235, v95
	v_fma_f32 v95, -0.5, v214, v233
	v_med3_f32 v95, v95, s94, v180
	v_mul_f32_e32 v230, 0x3fb8aa3b, v95
	v_mul_f32_e32 v95, 0xbfb8aa3b, v95
	v_mul_f32_e32 v97, v231, v97
	v_exp_f32_e32 v230, v230
	v_exp_f32_e32 v95, v95
	v_mul_f32_e32 v231, 0x3fb8aa3b, v233
	v_exp_f32_e32 v231, v231
	v_mfma_f32_16x16x32_bf16 v[98:101], v[98:101], v[102:105], 0
	v_mul_f32_e32 v94, 0x3e000000, v94
	v_mul_f32_e32 v233, v94, v230
	v_mul_f32_e32 v230, v232, v95
	v_mul_f32_e32 v244, v94, v231
	v_cvt_pk_bf16_f32 v94, v78, v79
	v_cvt_pk_bf16_f32 v95, v74, v75
	v_cvt_pk_bf16_f32 v96, v229, v96
	v_cvt_pk_bf16_f32 v97, v97, v230
	v_cvt_pk_bf16_f32 v230, v183, v184
	v_cvt_pk_bf16_f32 v231, v185, v238
	v_cvt_pk_bf16_f32 v232, v240, v239
	v_cvt_pk_bf16_f32 v233, v241, v233
	v_mov_b32_e32 v3, v2
	v_mfma_f32_16x16x32_bf16 v[94:97], v[94:97], v[230:233], v[98:101]
	v_mov_b32_e32 v232, v2
	v_mov_b32_e32 v233, v2
	v_cvt_pk_bf16_f32 v234, v82, v83
	v_cvt_pk_bf16_f32 v235, v182, v237
	v_cvt_pk_bf16_f32 v236, v236, v242
	v_cvt_pk_bf16_f32 v237, v243, v244
	s_nop 5
	v_cndmask_b32_e64 v74, v94, 0, s[40:41]
	v_cndmask_b32_e64 v75, 0, v95, s[42:43]
	v_cndmask_b32_e64 v78, v96, 0, s[44:45]
	v_cndmask_b32_e64 v79, v97, 0, s[46:47]
	v_cvt_pk_bf16_f32 v230, v74, v75
	v_cvt_pk_bf16_f32 v231, v78, v79
	v_cvt_pk_bf16_f32 v98, v4, v5
	v_cvt_pk_bf16_f32 v99, v6, v7
	v_cvt_pk_bf16_f32 v100, v20, v21
	v_cvt_pk_bf16_f32 v101, v22, v23
	v_mov_b32_e32 v82, v2
	v_mfma_f32_16x16x32_bf16 v[94:97], v[230:233], v[0:3], 0
	v_mov_b32_e32 v83, v2
	v_mov_b32_e32 v78, v2
	v_mov_b32_e32 v79, v2
	v_mfma_f32_16x16x32_bf16 v[94:97], v[106:109], v[98:101], v[94:97]
	v_cvt_pk_bf16_f32 v98, v32, v33
	v_cvt_pk_bf16_f32 v99, v34, v35
	v_cvt_pk_bf16_f32 v100, v52, v53
	v_cvt_pk_bf16_f32 v101, v54, v55
	v_cvt_pk_bf16_f32 v102, v8, v9
	v_cvt_pk_bf16_f32 v103, v10, v11
	v_cvt_pk_bf16_f32 v104, v24, v25
	v_cvt_pk_bf16_f32 v105, v26, v27
	v_mov_b32_e32 v74, v2
	v_mfma_f32_16x16x32_bf16 v[94:97], v[234:237], v[98:101], v[94:97]
	v_mov_b32_e32 v75, v2
	s_mov_b64 s[6:7], -1
	s_and_b64 vcc, exec, s[4:5]
	v_mfma_f32_16x16x32_bf16 v[98:101], v[230:233], v[80:83], 0
	v_mfma_f32_16x16x32_bf16 v[98:101], v[106:109], v[102:105], v[98:101]
	v_cvt_pk_bf16_f32 v102, v36, v37
	v_cvt_pk_bf16_f32 v103, v38, v39
	v_cvt_pk_bf16_f32 v104, v56, v57
	v_cvt_pk_bf16_f32 v105, v58, v59
	v_cvt_pk_bf16_f32 v238, v12, v13
	v_cvt_pk_bf16_f32 v239, v14, v15
	v_cvt_pk_bf16_f32 v240, v28, v29
	v_cvt_pk_bf16_f32 v241, v30, v31
	s_nop 0
	v_mfma_f32_16x16x32_bf16 v[98:101], v[234:237], v[102:105], v[98:101]
	v_mfma_f32_16x16x32_bf16 v[102:105], v[230:233], v[76:79], 0
	v_mfma_f32_16x16x32_bf16 v[102:105], v[106:109], v[238:241], v[102:105]
	v_cvt_pk_bf16_f32 v238, v40, v41
	v_cvt_pk_bf16_f32 v239, v42, v43
	v_cvt_pk_bf16_f32 v240, v60, v61
	v_mfma_f32_16x16x32_bf16 v[230:233], v[230:233], v[72:75], 0
	v_cvt_pk_bf16_f32 v241, v62, v63
	s_nop 0
	v_mfma_f32_16x16x32_bf16 v[102:105], v[234:237], v[238:241], v[102:105]
	v_cvt_pk_bf16_f32 v238, v16, v17
	v_cvt_pk_bf16_f32 v239, v18, v19
	v_cvt_pk_bf16_f32 v240, v48, v49
	v_cvt_pk_bf16_f32 v241, v50, v51
	s_nop 0
	v_mfma_f32_16x16x32_bf16 v[106:109], v[106:109], v[238:241], v[230:233]
	v_cvt_pk_bf16_f32 v230, v44, v45
	v_cvt_pk_bf16_f32 v231, v46, v47
	v_cvt_pk_bf16_f32 v232, v64, v65
	v_cvt_pk_bf16_f32 v233, v66, v67
	s_nop 3
	v_mfma_f32_16x16x32_bf16 v[106:109], v[234:237], v[230:233], v[106:109]
	s_cbranch_vccz .LBB0_1176
; __device__ __forceinline__ unsigned short f2bf(float f) { return (unsigned short)(cvt_pk_bf16(f, 0.f) & 0xffffu); }
; __device__ __forceinline__ float siluf_(float x) { return x * sigmoidf_(x); }
; template <bool WITHO, bool RAW = false>
; __device__ __forceinline__ void hg_pass(const Frame& F, const bf16_t* P, const float* lbh, int b, int h, int nb, int dir, f32x4 (&S)[4][4], float (&Gsum)[16],
;                                         LAS bf16_t* Vl, LAS bf16_t* Kl, float* OF, const float* ngp) {
;     ...
;                 { float tot[4][4], sq[4];
; #pragma unroll
;                 for (int i = 0; i < 4; ++i) { sq[i] = 0.f;
; #pragma unroll
;                     for (int vt = 0; vt < 4; ++vt) { tot[i][vt] = o[vt][i] + ofv[i][vt]; sq[i] = fmaf(tot[i][vt], tot[i][vt], sq[i]); } }
;                 ROW_ALLREDUCE4(sq[0], sq[1], sq[2], sq[3]);
; #pragma unroll
;                 for (int i = 0; i < 4; ++i) { const float rs = rsqrtf(sq[i] * (1.0f / 64.0f) + 1e-6f);
; #pragma unroll
;                     for (int vt = 0; vt < 4; ++vt) F.MIX[(size_t)orow[i] * DM + 512 + h * 64 + 16 * vt + tau] = f2bf(tot[i][vt] * rs * ngv[vt] * siluf_(gtv[i][vt])); } }
	v_add_f32_e32 v182, v207, v94
	v_add_f32_e32 v240, v197, v95
	v_add_f32_e32 v245, v201, v96
	v_add_f32_e32 v232, v205, v97
	v_fma_f32 v183, v182, v182, 0
	v_add_f32_e32 v184, v208, v98
	v_fma_f32 v241, v240, v240, 0
	v_add_f32_e32 v242, v198, v99
	v_fma_f32 v246, v245, v245, 0
	v_add_f32_e32 v236, v202, v100
	v_fma_f32 v233, v232, v232, 0
	v_add_f32_e32 v231, v206, v101
	v_fmac_f32_e32 v183, v184, v184
	v_add_f32_e32 v185, v210, v102
	v_fmac_f32_e32 v241, v242, v242
	v_add_f32_e32 v243, v199, v103
	v_fmac_f32_e32 v246, v236, v236
	v_add_f32_e32 v235, v203, v104
	v_fmac_f32_e32 v233, v231, v231
	v_add_f32_e32 v230, v209, v105
	v_fmac_f32_e32 v183, v185, v185
	v_add_f32_e32 v237, v211, v106
	v_fmac_f32_e32 v241, v243, v243
	v_add_f32_e32 v244, v200, v107
	v_fmac_f32_e32 v246, v235, v235
	v_add_f32_e32 v234, v204, v108
	v_fmac_f32_e32 v233, v230, v230
	v_add_f32_e32 v229, v212, v109
	v_fmac_f32_e32 v183, v237, v237
	v_fmac_f32_e32 v241, v244, v244
	v_fmac_f32_e32 v246, v234, v234
	v_fmac_f32_e32 v233, v229, v229
	s_nop 1
	v_add_f32_dpp v183, v183, v183 quad_perm:[1,0,3,2] row_mask:0xf bank_mask:0xf
	v_add_f32_dpp v241, v241, v241 quad_perm:[1,0,3,2] row_mask:0xf bank_mask:0xf
	v_add_f32_dpp v246, v246, v246 quad_perm:[1,0,3,2] row_mask:0xf bank_mask:0xf
	v_add_f32_dpp v233, v233, v233 quad_perm:[1,0,3,2] row_mask:0xf bank_mask:0xf
	v_add_f32_dpp v183, v183, v183 quad_perm:[2,3,0,1] row_mask:0xf bank_mask:0xf
	v_add_f32_dpp v241, v241, v241 quad_perm:[2,3,0,1] row_mask:0xf bank_mask:0xf
	v_add_f32_dpp v246, v246, v246 quad_perm:[2,3,0,1] row_mask:0xf bank_mask:0xf
	v_add_f32_dpp v233, v233, v233 quad_perm:[2,3,0,1] row_mask:0xf bank_mask:0xf
	v_add_f32_dpp v183, v183, v183 row_half_mirror row_mask:0xf bank_mask:0xf
	v_add_f32_dpp v241, v241, v241 row_half_mirror row_mask:0xf bank_mask:0xf
	v_add_f32_dpp v246, v246, v246 row_half_mirror row_mask:0xf bank_mask:0xf
	v_add_f32_dpp v233, v233, v233 row_half_mirror row_mask:0xf bank_mask:0xf
	v_add_f32_dpp v183, v183, v183 row_mirror row_mask:0xf bank_mask:0xf
	v_add_f32_dpp v241, v241, v241 row_mirror row_mask:0xf bank_mask:0xf
	v_add_f32_dpp v246, v246, v246 row_mirror row_mask:0xf bank_mask:0xf
	v_add_f32_dpp v233, v233, v233 row_mirror row_mask:0xf bank_mask:0xf
	s_mov_b64 s[6:7], 0
	v_fmamk_f32 v183, v183, 0x3c800000, v175
	v_cmp_gt_f32_e32 vcc, s92, v183
	v_mul_f32_e32 v238, 0x4b800000, v183
	s_nop 0
	v_cndmask_b32_e32 v183, v183, v238, vcc
	v_rsq_f32_e32 v183, v183
	s_nop 0
	v_mul_f32_e32 v238, 0x45800000, v183
	v_cndmask_b32_e32 v183, v183, v238, vcc
	v_mul_f32_e32 v238, 0xbfb8aa3b, v167
	v_exp_f32_e32 v238, v238
	v_mul_f32_e32 v182, v182, v183
	s_waitcnt lgkmcnt(0)
; __device__ __forceinline__ unsigned short f2bf(float f) { return (unsigned short)(cvt_pk_bf16(f, 0.f) & 0xffffu); }
; __device__ __forceinline__ float siluf_(float x) { return x * sigmoidf_(x); }
; template <bool WITHO, bool RAW = false>
; __device__ __forceinline__ void hg_pass(const Frame& F, const bf16_t* P, const float* lbh, int b, int h, int nb, int dir, f32x4 (&S)[4][4], float (&Gsum)[16],
;                                         LAS bf16_t* Vl, LAS bf16_t* Kl, float* OF, const float* ngp) {
;     ...
;                 { float tot[4][4], sq[4];
; #pragma unroll
;                 for (int i = 0; i < 4; ++i) { sq[i] = 0.f;
; #pragma unroll
;                     for (int vt = 0; vt < 4; ++vt) { tot[i][vt] = o[vt][i] + ofv[i][vt]; sq[i] = fmaf(tot[i][vt], tot[i][vt], sq[i]); } }
;                 ROW_ALLREDUCE4(sq[0], sq[1], sq[2], sq[3]);
; #pragma unroll
;                 for (int i = 0; i < 4; ++i) { const float rs = rsqrtf(sq[i] * (1.0f / 64.0f) + 1e-6f);
; #pragma unroll
;                     for (int vt = 0; vt < 4; ++vt) F.MIX[(size_t)orow[i] * DM + 512 + h * 64 + 16 * vt + tau] = f2bf(tot[i][vt] * rs * ngv[vt] * siluf_(gtv[i][vt])); } }
	v_mul_f32_e32 v182, v196, v182
	v_add_f32_e32 v238, 1.0, v238
	v_rcp_f32_e32 v238, v238
	s_nop 0
	v_mul_f32_e32 v238, v167, v238
	v_mul_f32_e32 v182, v238, v182
	v_lshlrev_b64 v[238:239], 11, v[172:173]
	v_cvt_pk_bf16_f32 v182, v182, v2
	v_lshl_add_u64 v[238:239], v[134:135], 0, v[238:239]
	global_store_short v[238:239], v182, off offset:1024
	v_mul_f32_e32 v182, v184, v183
	v_mul_f32_e32 v184, 0xbfb8aa3b, v166
	v_exp_f32_e32 v184, v184
	v_mul_f32_e32 v182, v195, v182
	v_add_f32_e32 v184, 1.0, v184
	v_rcp_f32_e32 v184, v184
	s_nop 0
	v_mul_f32_e32 v184, v166, v184
	v_mul_f32_e32 v182, v184, v182
	v_mul_f32_e32 v184, 0xbfb8aa3b, v169
	v_exp_f32_e32 v184, v184
	v_cvt_pk_bf16_f32 v182, v182, v2
	global_store_short v[238:239], v182, off offset:1056
	v_mul_f32_e32 v182, v185, v183
	v_add_f32_e32 v184, 1.0, v184
	v_rcp_f32_e32 v184, v184
	v_mul_f32_e32 v182, v194, v182
	v_mul_f32_e32 v184, v169, v184
	v_mul_f32_e32 v182, v184, v182
	v_cvt_pk_bf16_f32 v182, v182, v2
	global_store_short v[238:239], v182, off offset:1088
	v_mul_f32_e32 v182, v237, v183
	v_mul_f32_e32 v183, 0xbfb8aa3b, v168
	v_exp_f32_e32 v183, v183
	v_mul_f32_e32 v182, v125, v182
	v_mul_f32_e32 v184, 0xbfb8aa3b, v157
	v_exp_f32_e32 v184, v184
	v_add_f32_e32 v183, 1.0, v183
	v_rcp_f32_e32 v183, v183
	v_add_f32_e32 v184, 1.0, v184
	v_rcp_f32_e32 v184, v184
	v_mul_f32_e32 v183, v168, v183
	v_mul_f32_e32 v182, v183, v182
	v_cvt_pk_bf16_f32 v182, v182, v2
	global_store_short v[238:239], v182, off offset:1120
	v_fmamk_f32 v182, v241, 0x3c800000, v175
	v_cmp_gt_f32_e32 vcc, s92, v182
	v_mul_f32_e32 v183, 0x4b800000, v182
	v_mul_f32_e32 v184, v157, v184
	v_cndmask_b32_e32 v182, v182, v183, vcc
	v_rsq_f32_e32 v182, v182
	v_lshlrev_b64 v[238:239], 11, v[90:91]
	v_lshl_add_u64 v[238:239], v[134:135], 0, v[238:239]
	v_mul_f32_e32 v183, 0x45800000, v182
	v_cndmask_b32_e32 v182, v182, v183, vcc
	v_mul_f32_e32 v183, v240, v182
	v_mul_f32_e32 v183, v196, v183
	v_mul_f32_e32 v183, v184, v183
	v_mul_f32_e32 v184, 0xbfb8aa3b, v156
	v_exp_f32_e32 v184, v184
	v_cvt_pk_bf16_f32 v183, v183, v2
	global_store_short v[238:239], v183, off offset:1024
	v_mul_f32_e32 v183, v242, v182
	v_add_f32_e32 v184, 1.0, v184
	v_rcp_f32_e32 v184, v184
	v_mul_f32_e32 v183, v195, v183
	v_mul_f32_e32 v184, v156, v184
	v_mul_f32_e32 v183, v184, v183
	v_mul_f32_e32 v184, 0xbfb8aa3b, v159
	v_exp_f32_e32 v184, v184
	v_cvt_pk_bf16_f32 v183, v183, v2
	global_store_short v[238:239], v183, off offset:1056
	v_mul_f32_e32 v183, v243, v182
	v_add_f32_e32 v184, 1.0, v184
	v_rcp_f32_e32 v184, v184
	v_mul_f32_e32 v183, v194, v183
	v_mul_f32_e32 v182, v244, v182
	v_mul_f32_e32 v182, v125, v182
	v_mul_f32_e32 v184, v159, v184
	v_mul_f32_e32 v183, v184, v183
	v_cvt_pk_bf16_f32 v183, v183, v2
	global_store_short v[238:239], v183, off offset:1088
	v_mul_f32_e32 v183, 0xbfb8aa3b, v158
	v_exp_f32_e32 v183, v183
	v_mul_f32_e32 v184, 0xbfb8aa3b, v161
	v_exp_f32_e32 v184, v184
	v_add_f32_e32 v183, 1.0, v183
	v_rcp_f32_e32 v183, v183
	v_add_f32_e32 v184, 1.0, v184
	v_rcp_f32_e32 v184, v184
	v_mul_f32_e32 v183, v158, v183
	v_mul_f32_e32 v182, v183, v182
	v_cvt_pk_bf16_f32 v182, v182, v2
	global_store_short v[238:239], v182, off offset:1120
	v_fmamk_f32 v182, v246, 0x3c800000, v175
	v_cmp_gt_f32_e32 vcc, s92, v182
	v_mul_f32_e32 v183, 0x4b800000, v182
	v_mul_f32_e32 v184, v161, v184
	v_cndmask_b32_e32 v182, v182, v183, vcc
	v_rsq_f32_e32 v182, v182
	v_lshlrev_b64 v[238:239], 11, v[86:87]
	v_lshl_add_u64 v[238:239], v[134:135], 0, v[238:239]
	v_mul_f32_e32 v183, 0x45800000, v182
	v_cndmask_b32_e32 v182, v182, v183, vcc
	v_mul_f32_e32 v183, v245, v182
	v_mul_f32_e32 v183, v196, v183
	v_mul_f32_e32 v183, v184, v183
	v_mul_f32_e32 v184, 0xbfb8aa3b, v160
	v_exp_f32_e32 v184, v184
	v_cvt_pk_bf16_f32 v183, v183, v2
	global_store_short v[238:239], v183, off offset:1024
	v_mul_f32_e32 v183, v236, v182
	v_add_f32_e32 v184, 1.0, v184
	v_rcp_f32_e32 v184, v184
	v_mul_f32_e32 v183, v195, v183
	v_mul_f32_e32 v184, v160, v184
	v_mul_f32_e32 v183, v184, v183
	v_mul_f32_e32 v184, 0xbfb8aa3b, v162
	v_exp_f32_e32 v184, v184
	v_cvt_pk_bf16_f32 v183, v183, v2
	global_store_short v[238:239], v183, off offset:1056
	v_mul_f32_e32 v183, v235, v182
	v_add_f32_e32 v184, 1.0, v184
	v_rcp_f32_e32 v184, v184
	v_mul_f32_e32 v183, v194, v183
	v_mul_f32_e32 v182, v234, v182
	v_mul_f32_e32 v182, v125, v182
	v_mul_f32_e32 v184, v162, v184
	v_mul_f32_e32 v183, v184, v183
	v_cvt_pk_bf16_f32 v183, v183, v2
	global_store_short v[238:239], v183, off offset:1088
	v_mul_f32_e32 v183, 0xbfb8aa3b, v163
	v_exp_f32_e32 v183, v183
	v_mul_f32_e32 v184, 0xbfb8aa3b, v164
	v_exp_f32_e32 v184, v184
	v_add_f32_e32 v183, 1.0, v183
	v_rcp_f32_e32 v183, v183
	v_add_f32_e32 v184, 1.0, v184
	v_rcp_f32_e32 v184, v184
	v_mul_f32_e32 v183, v163, v183
	v_mul_f32_e32 v182, v183, v182
	v_cvt_pk_bf16_f32 v182, v182, v2
	global_store_short v[238:239], v182, off offset:1120
	v_fmamk_f32 v182, v233, 0x3c800000, v175
	v_cmp_gt_f32_e32 vcc, s92, v182
	v_mul_f32_e32 v183, 0x4b800000, v182
	v_mul_f32_e32 v184, v164, v184
	v_cndmask_b32_e32 v182, v182, v183, vcc
	v_rsq_f32_e32 v182, v182
	s_nop 0
	v_mul_f32_e32 v183, 0x45800000, v182
	v_cndmask_b32_e32 v182, v182, v183, vcc
	v_mul_f32_e32 v183, v232, v182
	v_mul_f32_e32 v183, v196, v183
	v_mul_f32_e32 v183, v184, v183
	v_mul_f32_e32 v184, 0xbfb8aa3b, v165
	v_exp_f32_e32 v184, v184
	v_lshlrev_b64 v[232:233], 11, v[70:71]
	v_cvt_pk_bf16_f32 v183, v183, v2
	v_lshl_add_u64 v[232:233], v[134:135], 0, v[232:233]
	v_add_f32_e32 v184, 1.0, v184
	v_rcp_f32_e32 v184, v184
	global_store_short v[232:233], v183, off offset:1024
	v_mul_f32_e32 v183, v231, v182
	v_mul_f32_e32 v183, v195, v183
	v_mul_f32_e32 v184, v165, v184
	v_mul_f32_e32 v183, v184, v183
	v_mul_f32_e32 v184, 0xbfb8aa3b, v170
	v_exp_f32_e32 v184, v184
	v_cvt_pk_bf16_f32 v183, v183, v2
	global_store_short v[232:233], v183, off offset:1056
	v_mul_f32_e32 v183, v230, v182
	v_add_f32_e32 v184, 1.0, v184
	v_rcp_f32_e32 v184, v184
	v_mul_f32_e32 v183, v194, v183
	v_mul_f32_e32 v182, v229, v182
	v_mul_f32_e32 v182, v125, v182
	v_mul_f32_e32 v184, v170, v184
	v_mul_f32_e32 v183, v184, v183
	v_cvt_pk_bf16_f32 v183, v183, v2
	global_store_short v[232:233], v183, off offset:1088
	v_mul_f32_e32 v183, 0xbfb8aa3b, v171
	v_exp_f32_e32 v183, v183
	s_nop 0
	v_add_f32_e32 v183, 1.0, v183
	v_rcp_f32_e32 v183, v183
	s_nop 0
	v_mul_f32_e32 v183, v171, v183
	v_mul_f32_e32 v182, v183, v182
	v_cvt_pk_bf16_f32 v182, v182, v2
	global_store_short v[232:233], v182, off offset:1120
